# persistent hop kernels: rows grouped by degree, 2 proportional column sweeps; K3 scatters in 4 column-quarter passes
# speedup vs baseline: 1.0548x; 1.0548x over previous
.LBB2_108:
	s_and_b64 vcc, exec, s[0:1]
	s_cbranch_vccz .LBB2_129
	s_mov_b32 s58, 0x29f17
	v_mov_b32_e32 v80, 1
	v_and_b32_e32 v64, 0x1ffff, v30
	v_mul_hi_u32 v64, v64, s58
	v_and_b32_e32 v65, 0x1ffff, v32
	v_mul_hi_u32 v65, v65, s58
	v_and_b32_e32 v66, 0x1ffff, v18
	v_mul_hi_u32 v66, v66, s58
	v_and_b32_e32 v67, 0x1ffff, v20
	v_mul_hi_u32 v67, v67, s58
	v_and_b32_e32 v68, 0x1ffff, v26
	v_mul_hi_u32 v68, v68, s58
	v_and_b32_e32 v69, 0x1ffff, v28
	v_mul_hi_u32 v69, v69, s58
	v_and_b32_e32 v70, 0x1ffff, v10
	v_mul_hi_u32 v70, v70, s58
	v_and_b32_e32 v71, 0x1ffff, v12
	v_mul_hi_u32 v71, v71, s58
	v_and_b32_e32 v72, 0x1ffff, v22
	v_mul_hi_u32 v72, v72, s58
	v_and_b32_e32 v73, 0x1ffff, v24
	v_mul_hi_u32 v73, v73, s58
	v_and_b32_e32 v74, 0x1ffff, v6
	v_mul_hi_u32 v74, v74, s58
	v_and_b32_e32 v75, 0x1ffff, v8
	v_mul_hi_u32 v75, v75, s58
	v_and_b32_e32 v76, 0x1ffff, v14
	v_mul_hi_u32 v76, v76, s58
	v_and_b32_e32 v77, 0x1ffff, v16
	v_mul_hi_u32 v77, v77, s58
	v_and_b32_e32 v78, 0x1ffff, v2
	v_mul_hi_u32 v78, v78, s58
	v_and_b32_e32 v79, 0x1ffff, v4
	v_mul_hi_u32 v79, v79, s58
	s_mov_b32 s59, 0
.Lk3_pass:
	v_cmp_eq_u32_e64 s[60:61], s59, v64
	s_and_b64 s[60:61], s[60:61], s[30:31]
	v_cmp_eq_u32_e64 s[62:63], s59, v65
	s_and_b64 s[62:63], s[62:63], s[28:29]
	v_cmp_eq_u32_e64 s[64:65], s59, v66
	s_and_b64 s[64:65], s[64:65], s[26:27]
	v_cmp_eq_u32_e64 s[66:67], s59, v67
	s_and_b64 s[66:67], s[66:67], s[24:25]
	v_cmp_eq_u32_e64 s[68:69], s59, v68
	s_and_b64 s[68:69], s[68:69], s[22:23]
	v_cmp_eq_u32_e64 s[70:71], s59, v69
	s_and_b64 s[70:71], s[70:71], s[20:21]
	v_cmp_eq_u32_e64 s[72:73], s59, v70
	s_and_b64 s[72:73], s[72:73], s[18:19]
	v_cmp_eq_u32_e64 s[74:75], s59, v71
	s_and_b64 s[74:75], s[74:75], s[16:17]
	v_cmp_eq_u32_e64 s[76:77], s59, v72
	s_and_b64 s[76:77], s[76:77], s[14:15]
	v_cmp_eq_u32_e64 s[78:79], s59, v73
	s_and_b64 s[78:79], s[78:79], s[12:13]
	v_cmp_eq_u32_e64 s[80:81], s59, v74
	s_and_b64 s[80:81], s[80:81], s[10:11]
	v_cmp_eq_u32_e64 s[82:83], s59, v75
	s_and_b64 s[82:83], s[82:83], s[8:9]
	v_cmp_eq_u32_e64 s[84:85], s59, v76
	s_and_b64 s[84:85], s[84:85], s[6:7]
	v_cmp_eq_u32_e64 s[86:87], s59, v77
	s_and_b64 s[86:87], s[86:87], s[4:5]
	v_cmp_eq_u32_e64 s[88:89], s59, v78
	s_and_b64 s[88:89], s[88:89], s[2:3]
	v_cmp_eq_u32_e64 s[90:91], s59, v79
	s_and_b64 s[90:91], s[90:91], s[34:35]
	s_mov_b64 exec, s[60:61]
	v_lshrrev_b32_e32 v48, 15, v30
	v_and_b32_e32 v48, 0x1fffc, v48
	v_add_u32_e32 v48, 0x10000, v48
	ds_add_rtn_u32 v48, v48, v80
	s_mov_b64 exec, s[62:63]
	v_lshrrev_b32_e32 v49, 15, v32
	v_and_b32_e32 v49, 0x1fffc, v49
	v_add_u32_e32 v49, 0x10000, v49
	ds_add_rtn_u32 v49, v49, v80
	s_mov_b64 exec, s[64:65]
	v_lshrrev_b32_e32 v50, 15, v18
	v_and_b32_e32 v50, 0x1fffc, v50
	v_add_u32_e32 v50, 0x10000, v50
	ds_add_rtn_u32 v50, v50, v80
	s_mov_b64 exec, s[66:67]
	v_lshrrev_b32_e32 v51, 15, v20
	v_and_b32_e32 v51, 0x1fffc, v51
	v_add_u32_e32 v51, 0x10000, v51
	ds_add_rtn_u32 v51, v51, v80
	s_mov_b64 exec, s[68:69]
	v_lshrrev_b32_e32 v52, 15, v26
	v_and_b32_e32 v52, 0x1fffc, v52
	v_add_u32_e32 v52, 0x10000, v52
	ds_add_rtn_u32 v52, v52, v80
	s_mov_b64 exec, s[70:71]
	v_lshrrev_b32_e32 v53, 15, v28
	v_and_b32_e32 v53, 0x1fffc, v53
	v_add_u32_e32 v53, 0x10000, v53
	ds_add_rtn_u32 v53, v53, v80
	s_mov_b64 exec, s[72:73]
	v_lshrrev_b32_e32 v54, 15, v10
	v_and_b32_e32 v54, 0x1fffc, v54
	v_add_u32_e32 v54, 0x10000, v54
	ds_add_rtn_u32 v54, v54, v80
	s_mov_b64 exec, s[74:75]
	v_lshrrev_b32_e32 v55, 15, v12
	v_and_b32_e32 v55, 0x1fffc, v55
	v_add_u32_e32 v55, 0x10000, v55
	ds_add_rtn_u32 v55, v55, v80
	s_mov_b64 exec, s[76:77]
	v_lshrrev_b32_e32 v56, 15, v22
	v_and_b32_e32 v56, 0x1fffc, v56
	v_add_u32_e32 v56, 0x10000, v56
	ds_add_rtn_u32 v56, v56, v80
	s_mov_b64 exec, s[78:79]
	v_lshrrev_b32_e32 v57, 15, v24
	v_and_b32_e32 v57, 0x1fffc, v57
	v_add_u32_e32 v57, 0x10000, v57
	ds_add_rtn_u32 v57, v57, v80
	s_mov_b64 exec, s[80:81]
	v_lshrrev_b32_e32 v58, 15, v6
	v_and_b32_e32 v58, 0x1fffc, v58
	v_add_u32_e32 v58, 0x10000, v58
	ds_add_rtn_u32 v58, v58, v80
	s_mov_b64 exec, s[82:83]
	v_lshrrev_b32_e32 v59, 15, v8
	v_and_b32_e32 v59, 0x1fffc, v59
	v_add_u32_e32 v59, 0x10000, v59
	ds_add_rtn_u32 v59, v59, v80
	s_waitcnt lgkmcnt(8)
	s_mov_b64 exec, s[84:85]
	v_lshrrev_b32_e32 v60, 15, v14
	v_and_b32_e32 v60, 0x1fffc, v60
	v_add_u32_e32 v60, 0x10000, v60
	ds_add_rtn_u32 v60, v60, v80
	s_mov_b64 exec, s[86:87]
	v_lshrrev_b32_e32 v61, 15, v16
	v_and_b32_e32 v61, 0x1fffc, v61
	v_add_u32_e32 v61, 0x10000, v61
	ds_add_rtn_u32 v61, v61, v80
	s_mov_b64 exec, s[88:89]
	v_lshrrev_b32_e32 v62, 15, v2
	v_and_b32_e32 v62, 0x1fffc, v62
	v_add_u32_e32 v62, 0x10000, v62
	ds_add_rtn_u32 v62, v62, v80
	s_mov_b64 exec, s[90:91]
	v_lshrrev_b32_e32 v63, 15, v4
	v_and_b32_e32 v63, 0x1fffc, v63
	v_add_u32_e32 v63, 0x10000, v63
	ds_add_rtn_u32 v63, v63, v80
	s_waitcnt lgkmcnt(0)
	s_mov_b64 exec, s[60:61]
	v_and_b32_e32 v30, 0x1ffff, v30
	v_lshlrev_b32_e32 v48, 3, v48
	ds_write_b64 v48, v[30:31]
	s_mov_b64 exec, s[62:63]
	v_and_b32_e32 v32, 0x1ffff, v32
	v_lshlrev_b32_e32 v49, 3, v49
	ds_write_b64 v49, v[32:33]
	s_mov_b64 exec, s[64:65]
	v_and_b32_e32 v18, 0x1ffff, v18
	v_lshlrev_b32_e32 v50, 3, v50
	ds_write_b64 v50, v[18:19]
	s_mov_b64 exec, s[66:67]
	v_and_b32_e32 v20, 0x1ffff, v20
	v_lshlrev_b32_e32 v51, 3, v51
	ds_write_b64 v51, v[20:21]
	s_mov_b64 exec, s[68:69]
	v_and_b32_e32 v26, 0x1ffff, v26
	v_lshlrev_b32_e32 v52, 3, v52
	ds_write_b64 v52, v[26:27]
	s_mov_b64 exec, s[70:71]
	v_and_b32_e32 v28, 0x1ffff, v28
	v_lshlrev_b32_e32 v53, 3, v53
	ds_write_b64 v53, v[28:29]
	s_mov_b64 exec, s[72:73]
	v_and_b32_e32 v10, 0x1ffff, v10
	v_lshlrev_b32_e32 v54, 3, v54
	ds_write_b64 v54, v[10:11]
	s_mov_b64 exec, s[74:75]
	v_and_b32_e32 v12, 0x1ffff, v12
	v_lshlrev_b32_e32 v55, 3, v55
	ds_write_b64 v55, v[12:13]
	s_mov_b64 exec, s[76:77]
	v_and_b32_e32 v22, 0x1ffff, v22
	v_lshlrev_b32_e32 v56, 3, v56
	ds_write_b64 v56, v[22:23]
	s_mov_b64 exec, s[78:79]
	v_and_b32_e32 v24, 0x1ffff, v24
	v_lshlrev_b32_e32 v57, 3, v57
	ds_write_b64 v57, v[24:25]
	s_mov_b64 exec, s[80:81]
	v_and_b32_e32 v6, 0x1ffff, v6
	v_lshlrev_b32_e32 v58, 3, v58
	ds_write_b64 v58, v[6:7]
	s_mov_b64 exec, s[82:83]
	v_and_b32_e32 v8, 0x1ffff, v8
	v_lshlrev_b32_e32 v59, 3, v59
	ds_write_b64 v59, v[8:9]
	s_waitcnt lgkmcnt(8)
	s_mov_b64 exec, s[84:85]
	v_and_b32_e32 v14, 0x1ffff, v14
	v_lshlrev_b32_e32 v60, 3, v60
	ds_write_b64 v60, v[14:15]
	s_mov_b64 exec, s[86:87]
	v_and_b32_e32 v16, 0x1ffff, v16
	v_lshlrev_b32_e32 v61, 3, v61
	ds_write_b64 v61, v[16:17]
	s_mov_b64 exec, s[88:89]
	v_and_b32_e32 v2, 0x1ffff, v2
	v_lshlrev_b32_e32 v62, 3, v62
	ds_write_b64 v62, v[2:3]
	s_mov_b64 exec, s[90:91]
	v_and_b32_e32 v4, 0x1ffff, v4
	v_lshlrev_b32_e32 v63, 3, v63
	ds_write_b64 v63, v[4:5]
	s_mov_b64 exec, -1
	s_waitcnt lgkmcnt(0)
	s_barrier
	s_add_i32 s59, s59, 1
	s_cmp_lt_u32 s59, 4
	s_cbranch_scc1 .Lk3_pass

	.amdhsa_kernel _Z13k_bucket_sortPKiPK15HIP_vector_typeIiLj2EEPiPS2_
		.amdhsa_group_segment_fixed_size 67616
		.amdhsa_private_segment_fixed_size 0
		.amdhsa_kernarg_size 32
		.amdhsa_user_sgpr_count 2
		.amdhsa_user_sgpr_dispatch_ptr 0
		.amdhsa_user_sgpr_queue_ptr 0
		.amdhsa_user_sgpr_kernarg_segment_ptr 1
		.amdhsa_user_sgpr_dispatch_id 0
		.amdhsa_user_sgpr_kernarg_preload_length 0
		.amdhsa_user_sgpr_kernarg_preload_offset 0
		.amdhsa_user_sgpr_private_segment_size 0
		.amdhsa_uses_dynamic_stack 0
		.amdhsa_enable_private_segment 0
		.amdhsa_system_sgpr_workgroup_id_x 1
		.amdhsa_system_sgpr_workgroup_id_y 0
		.amdhsa_system_sgpr_workgroup_id_z 0
		.amdhsa_system_sgpr_workgroup_info 0
		.amdhsa_system_vgpr_workitem_id 0
		.amdhsa_next_free_vgpr 97
		.amdhsa_next_free_sgpr 96
		.amdhsa_accum_offset 96
		.amdhsa_reserve_vcc 1
		.amdhsa_float_round_mode_32 0
		.amdhsa_float_round_mode_16_64 0
		.amdhsa_float_denorm_mode_32 3
		.amdhsa_float_denorm_mode_16_64 3
		.amdhsa_dx10_clamp 1
		.amdhsa_ieee_mode 1
		.amdhsa_fp16_overflow 0
		.amdhsa_tg_split 0
		.amdhsa_exception_fp_ieee_invalid_op 0
		.amdhsa_exception_fp_denorm_src 0
		.amdhsa_exception_fp_ieee_div_zero 0
		.amdhsa_exception_fp_ieee_overflow 0
		.amdhsa_exception_fp_ieee_underflow 0
		.amdhsa_exception_fp_ieee_inexact 0
		.amdhsa_exception_int_div_zero 0
	.end_amdhsa_kernel

_Z5k_hopILi0EEvPKiPK15HIP_vector_typeIiLj2EEPKS2_IjLj4EEPS6_S8_S8_PKfSB_Pf:
	s_lshr_b32 s3, s2, 3
	s_cmpk_gt_u32 s3, 156
	s_cbranch_scc1 .Lhq0_exit
	s_load_dwordx4 s[4:7], s[0:1], 0x0
	s_load_dwordx4 s[8:11], s[0:1], 0x10
	v_lshrrev_b32_e32 v2, 6, v0
	v_and_b32_e32 v3, 63, v0
	s_bfe_u32 s13, s2, 0x10002
	s_and_b32 s14, s2, 3
	v_readfirstlane_b32 s12, v2
	s_lshl_b32 s15, s3, 2
	s_add_i32 s15, s15, s12
	s_mul_i32 s15, s15, 40
	s_mul_i32 s16, s14, 25000
	s_add_i32 s15, s15, s16
	s_add_i32 s16, s16, 24960
	s_min_u32 s15, s15, s16
	v_min_u32_e32 v4, 40, v3
	v_add_u32_e32 v4, s15, v4
	v_lshlrev_b32_e32 v4, 2, v4
	s_mul_i32 s17, s13, 0x61a84
	s_waitcnt lgkmcnt(0)
	s_add_u32 s4, s4, s17
	s_addc_u32 s5, s5, 0
	global_load_dword v5, v4, s[4:5]
	s_mul_i32 s17, s13, 0x927c00
	s_add_u32 s6, s6, s17
	s_addc_u32 s7, s7, 0
	s_mul_i32 s17, s13, 0xc35000
	s_add_u32 s8, s8, s17
	s_addc_u32 s9, s9, 0
	s_add_u32 s10, s10, s17
	s_addc_u32 s11, s11, 0
	s_mul_i32 s28, s12, 6976
	s_mov_b32 s29, 0xffff80
	v_and_b32_e32 v1, 7, v0
	v_lshlrev_b32_e32 v1, 4, v1
	v_lshrrev_b32_e32 v2, 3, v3
	v_lshlrev_b32_e32 v2, 2, v2
	v_lshlrev_b32_e32 v4, 3, v3
	v_add_u32_e32 v6, s28, v4
	v_add_u32_e32 v7, 1, v3
	v_lshlrev_b32_e32 v7, 2, v7
	s_waitcnt vmcnt(0)
	v_readlane_b32 s18, v5, 0
	v_readlane_b32 s19, v5, 40
	ds_bpermute_b32 v8, v7, v5
	s_sub_i32 s20, s19, s18
	s_lshl_b32 s21, s18, 3
	s_add_u32 s22, s6, s21
	s_addc_u32 s23, s7, 0
	s_add_u32 s24, s22, 0x1000
	s_addc_u32 s25, s23, 0
	s_cmpk_gt_i32 s20, 832
	s_cbranch_scc1 .Lhq0_staged
	global_load_dwordx2 v[56:57], v4, s[22:23] offset:0 nt
	s_cmpk_le_i32 s20, 64
	s_cbranch_scc1 .Lhq0_staged
	global_load_dwordx2 v[58:59], v4, s[22:23] offset:512 nt
	s_cmpk_le_i32 s20, 128
	s_cbranch_scc1 .Lhq0_staged
	global_load_dwordx2 v[60:61], v4, s[22:23] offset:1024 nt
	s_cmpk_le_i32 s20, 192
	s_cbranch_scc1 .Lhq0_staged
	global_load_dwordx2 v[62:63], v4, s[22:23] offset:1536 nt
	s_cmpk_le_i32 s20, 256
	s_cbranch_scc1 .Lhq0_staged
	global_load_dwordx2 v[64:65], v4, s[22:23] offset:2048 nt
	s_cmpk_le_i32 s20, 320
	s_cbranch_scc1 .Lhq0_staged
	global_load_dwordx2 v[66:67], v4, s[22:23] offset:2560 nt
	s_cmpk_le_i32 s20, 384
	s_cbranch_scc1 .Lhq0_staged
	global_load_dwordx2 v[68:69], v4, s[22:23] offset:3072 nt
	s_cmpk_le_i32 s20, 448
	s_cbranch_scc1 .Lhq0_staged
	global_load_dwordx2 v[70:71], v4, s[22:23] offset:3584 nt
	s_cmpk_le_i32 s20, 512
	s_cbranch_scc1 .Lhq0_staged
	global_load_dwordx2 v[72:73], v4, s[24:25] offset:0 nt
	s_cmpk_le_i32 s20, 576
	s_cbranch_scc1 .Lhq0_staged
	global_load_dwordx2 v[74:75], v4, s[24:25] offset:512 nt
	s_cmpk_le_i32 s20, 640
	s_cbranch_scc1 .Lhq0_staged
	global_load_dwordx2 v[76:77], v4, s[24:25] offset:1024 nt
	s_cmpk_le_i32 s20, 704
	s_cbranch_scc1 .Lhq0_staged
	global_load_dwordx2 v[78:79], v4, s[24:25] offset:1536 nt
	s_cmpk_le_i32 s20, 768
	s_cbranch_scc1 .Lhq0_staged
	global_load_dwordx2 v[80:81], v4, s[24:25] offset:2048 nt
.Lhq0_staged:
	s_waitcnt lgkmcnt(0)
	v_sub_u32_e32 v8, v8, v5
	v_lshlrev_b32_e32 v8, 6, v8
	v_sub_u32_e32 v9, 63, v3
	v_or_b32_e32 v8, v8, v9
	v_cmp_gt_u32_e32 vcc, 40, v3
	s_nop 1
	v_cndmask_b32_e32 v8, 0, v8, vcc
	v_lshlrev_b32_e32 v9, 2, v3
	v_add_u32_e32 v9, s28, v9
	ds_write_b32 v9, v8
	v_mov_b32_e32 v10, s28
	v_mov_b32_e32 v11, 0
	ds_read_b128 v[12:15], v10 offset:0
	ds_read_b128 v[16:19], v10 offset:16
	s_waitcnt lgkmcnt(0)
	v_sub_u32_e32 v20, v8, v12
	v_lshrrev_b32_e32 v20, 31, v20
	v_add_u32_e32 v11, v11, v20
	v_sub_u32_e32 v20, v8, v13
	v_lshrrev_b32_e32 v20, 31, v20
	v_add_u32_e32 v11, v11, v20
	v_sub_u32_e32 v20, v8, v14
	v_lshrrev_b32_e32 v20, 31, v20
	v_add_u32_e32 v11, v11, v20
	v_sub_u32_e32 v20, v8, v15
	v_lshrrev_b32_e32 v20, 31, v20
	v_add_u32_e32 v11, v11, v20
	v_sub_u32_e32 v20, v8, v16
	v_lshrrev_b32_e32 v20, 31, v20
	v_add_u32_e32 v11, v11, v20
	v_sub_u32_e32 v20, v8, v17
	v_lshrrev_b32_e32 v20, 31, v20
	v_add_u32_e32 v11, v11, v20
	v_sub_u32_e32 v20, v8, v18
	v_lshrrev_b32_e32 v20, 31, v20
	v_add_u32_e32 v11, v11, v20
	v_sub_u32_e32 v20, v8, v19
	v_lshrrev_b32_e32 v20, 31, v20
	v_add_u32_e32 v11, v11, v20
	ds_read_b128 v[12:15], v10 offset:32
	ds_read_b128 v[16:19], v10 offset:48
	s_waitcnt lgkmcnt(0)
	v_sub_u32_e32 v20, v8, v12
	v_lshrrev_b32_e32 v20, 31, v20
	v_add_u32_e32 v11, v11, v20
	v_sub_u32_e32 v20, v8, v13
	v_lshrrev_b32_e32 v20, 31, v20
	v_add_u32_e32 v11, v11, v20
	v_sub_u32_e32 v20, v8, v14
	v_lshrrev_b32_e32 v20, 31, v20
	v_add_u32_e32 v11, v11, v20
	v_sub_u32_e32 v20, v8, v15
	v_lshrrev_b32_e32 v20, 31, v20
	v_add_u32_e32 v11, v11, v20
	v_sub_u32_e32 v20, v8, v16
	v_lshrrev_b32_e32 v20, 31, v20
	v_add_u32_e32 v11, v11, v20
	v_sub_u32_e32 v20, v8, v17
	v_lshrrev_b32_e32 v20, 31, v20
	v_add_u32_e32 v11, v11, v20
	v_sub_u32_e32 v20, v8, v18
	v_lshrrev_b32_e32 v20, 31, v20
	v_add_u32_e32 v11, v11, v20
	v_sub_u32_e32 v20, v8, v19
	v_lshrrev_b32_e32 v20, 31, v20
	v_add_u32_e32 v11, v11, v20
	ds_read_b128 v[12:15], v10 offset:64
	ds_read_b128 v[16:19], v10 offset:80
	s_waitcnt lgkmcnt(0)
	v_sub_u32_e32 v20, v8, v12
	v_lshrrev_b32_e32 v20, 31, v20
	v_add_u32_e32 v11, v11, v20
	v_sub_u32_e32 v20, v8, v13
	v_lshrrev_b32_e32 v20, 31, v20
	v_add_u32_e32 v11, v11, v20
	v_sub_u32_e32 v20, v8, v14
	v_lshrrev_b32_e32 v20, 31, v20
	v_add_u32_e32 v11, v11, v20
	v_sub_u32_e32 v20, v8, v15
	v_lshrrev_b32_e32 v20, 31, v20
	v_add_u32_e32 v11, v11, v20
	v_sub_u32_e32 v20, v8, v16
	v_lshrrev_b32_e32 v20, 31, v20
	v_add_u32_e32 v11, v11, v20
	v_sub_u32_e32 v20, v8, v17
	v_lshrrev_b32_e32 v20, 31, v20
	v_add_u32_e32 v11, v11, v20
	v_sub_u32_e32 v20, v8, v18
	v_lshrrev_b32_e32 v20, 31, v20
	v_add_u32_e32 v11, v11, v20
	v_sub_u32_e32 v20, v8, v19
	v_lshrrev_b32_e32 v20, 31, v20
	v_add_u32_e32 v11, v11, v20
	ds_read_b128 v[12:15], v10 offset:96
	ds_read_b128 v[16:19], v10 offset:112
	s_waitcnt lgkmcnt(0)
	v_sub_u32_e32 v20, v8, v12
	v_lshrrev_b32_e32 v20, 31, v20
	v_add_u32_e32 v11, v11, v20
	v_sub_u32_e32 v20, v8, v13
	v_lshrrev_b32_e32 v20, 31, v20
	v_add_u32_e32 v11, v11, v20
	v_sub_u32_e32 v20, v8, v14
	v_lshrrev_b32_e32 v20, 31, v20
	v_add_u32_e32 v11, v11, v20
	v_sub_u32_e32 v20, v8, v15
	v_lshrrev_b32_e32 v20, 31, v20
	v_add_u32_e32 v11, v11, v20
	v_sub_u32_e32 v20, v8, v16
	v_lshrrev_b32_e32 v20, 31, v20
	v_add_u32_e32 v11, v11, v20
	v_sub_u32_e32 v20, v8, v17
	v_lshrrev_b32_e32 v20, 31, v20
	v_add_u32_e32 v11, v11, v20
	v_sub_u32_e32 v20, v8, v18
	v_lshrrev_b32_e32 v20, 31, v20
	v_add_u32_e32 v11, v11, v20
	v_sub_u32_e32 v20, v8, v19
	v_lshrrev_b32_e32 v20, 31, v20
	v_add_u32_e32 v11, v11, v20
	ds_read_b128 v[12:15], v10 offset:128
	ds_read_b128 v[16:19], v10 offset:144
	s_waitcnt lgkmcnt(0)
	v_sub_u32_e32 v20, v8, v12
	v_lshrrev_b32_e32 v20, 31, v20
	v_add_u32_e32 v11, v11, v20
	v_sub_u32_e32 v20, v8, v13
	v_lshrrev_b32_e32 v20, 31, v20
	v_add_u32_e32 v11, v11, v20
	v_sub_u32_e32 v20, v8, v14
	v_lshrrev_b32_e32 v20, 31, v20
	v_add_u32_e32 v11, v11, v20
	v_sub_u32_e32 v20, v8, v15
	v_lshrrev_b32_e32 v20, 31, v20
	v_add_u32_e32 v11, v11, v20
	v_sub_u32_e32 v20, v8, v16
	v_lshrrev_b32_e32 v20, 31, v20
	v_add_u32_e32 v11, v11, v20
	v_sub_u32_e32 v20, v8, v17
	v_lshrrev_b32_e32 v20, 31, v20
	v_add_u32_e32 v11, v11, v20
	v_sub_u32_e32 v20, v8, v18
	v_lshrrev_b32_e32 v20, 31, v20
	v_add_u32_e32 v11, v11, v20
	v_sub_u32_e32 v20, v8, v19
	v_lshrrev_b32_e32 v20, 31, v20
	v_add_u32_e32 v11, v11, v20
	v_cmp_gt_u32_e32 vcc, 40, v3
	s_and_saveexec_b64 s[44:45], vcc
	v_lshlrev_b32_e32 v11, 2, v11
	v_add_u32_e32 v11, s28, v11
	ds_write_b32 v11, v3 offset:6720
	s_mov_b64 exec, s[44:45]
	v_add_u32_e32 v9, s28, v2
	ds_read_b32 v12, v9 offset:6720
	ds_read_b32 v13, v9 offset:6752
	ds_read_b32 v14, v9 offset:6784
	ds_read_b32 v15, v9 offset:6816
	ds_read_b32 v16, v9 offset:6848
	s_waitcnt lgkmcnt(0)
	v_lshlrev_b32_e32 v12, 2, v12
	v_lshlrev_b32_e32 v13, 2, v13
	v_lshlrev_b32_e32 v14, 2, v14
	v_lshlrev_b32_e32 v15, 2, v15
	v_lshlrev_b32_e32 v16, 2, v16
	ds_bpermute_b32 v46, v12, v5
	ds_bpermute_b32 v51, v12, v5 offset:4
	ds_bpermute_b32 v47, v13, v5
	ds_bpermute_b32 v52, v13, v5 offset:4
	ds_bpermute_b32 v48, v14, v5
	ds_bpermute_b32 v53, v14, v5 offset:4
	ds_bpermute_b32 v49, v15, v5
	ds_bpermute_b32 v54, v15, v5 offset:4
	ds_bpermute_b32 v50, v16, v5
	ds_bpermute_b32 v55, v16, v5 offset:4
	s_waitcnt lgkmcnt(0)
	s_cmpk_gt_i32 s20, 832
	s_cbranch_scc1 .Lhq0_fallback
	s_waitcnt vmcnt(0)
	ds_write_b64 v6, v[56:57] offset:0
	ds_write_b64 v6, v[58:59] offset:512
	ds_write_b64 v6, v[60:61] offset:1024
	ds_write_b64 v6, v[62:63] offset:1536
	ds_write_b64 v6, v[64:65] offset:2048
	ds_write_b64 v6, v[66:67] offset:2560
	ds_write_b64 v6, v[68:69] offset:3072
	ds_write_b64 v6, v[70:71] offset:3584
	ds_write_b64 v6, v[72:73] offset:4096
	ds_write_b64 v6, v[74:75] offset:4608
	ds_write_b64 v6, v[76:77] offset:5120
	ds_write_b64 v6, v[78:79] offset:5632
	ds_write_b64 v6, v[80:81] offset:6144
	s_waitcnt lgkmcnt(0)
	v_subrev_u32_e32 v46, s18, v46
	v_subrev_u32_e32 v51, s18, v51
	v_lshl_add_u32 v46, v46, 3, s28
	v_lshl_add_u32 v51, v51, 3, s28
	v_subrev_u32_e32 v47, s18, v47
	v_subrev_u32_e32 v52, s18, v52
	v_lshl_add_u32 v47, v47, 3, s28
	v_lshl_add_u32 v52, v52, 3, s28
	v_subrev_u32_e32 v48, s18, v48
	v_subrev_u32_e32 v53, s18, v53
	v_lshl_add_u32 v48, v48, 3, s28
	v_lshl_add_u32 v53, v53, 3, s28
	v_subrev_u32_e32 v49, s18, v49
	v_subrev_u32_e32 v54, s18, v54
	v_lshl_add_u32 v49, v49, 3, s28
	v_lshl_add_u32 v54, v54, 3, s28
	v_subrev_u32_e32 v50, s18, v50
	v_subrev_u32_e32 v55, s18, v55
	v_lshl_add_u32 v50, v50, 3, s28
	v_lshl_add_u32 v55, v55, 3, s28
	v_mov_b32_e32 v56, 0
	v_mov_b32_e32 v57, 0
	v_mov_b32_e32 v58, 0
	v_mov_b32_e32 v59, 0
	v_mov_b32_e32 v60, 0
	v_mov_b32_e32 v61, 0
	v_mov_b32_e32 v62, 0
	v_mov_b32_e32 v63, 0
	v_mov_b32_e32 v64, 0
	v_mov_b32_e32 v65, 0
	v_mov_b32_e32 v66, 0
	v_mov_b32_e32 v67, 0
	v_mov_b32_e32 v68, 0
	v_mov_b32_e32 v69, 0
	v_mov_b32_e32 v70, 0
	v_mov_b32_e32 v71, 0
	v_mov_b32_e32 v72, 0
	v_mov_b32_e32 v73, 0
	v_mov_b32_e32 v74, 0
	v_mov_b32_e32 v75, 0
	v_mov_b32_e32 v76, 0
	v_mov_b32_e32 v77, 0
	v_mov_b32_e32 v78, 0
	v_mov_b32_e32 v79, 0
	v_mov_b32_e32 v80, 0
	v_mov_b32_e32 v81, 0
	v_mov_b32_e32 v82, 0
	v_mov_b32_e32 v83, 0
	v_mov_b32_e32 v84, 0
	v_mov_b32_e32 v85, 0
	v_mov_b32_e32 v86, 0
	v_mov_b32_e32 v87, 0
	v_mov_b32_e32 v88, 0
	v_mov_b32_e32 v89, 0
	v_mov_b32_e32 v90, 0
	v_mov_b32_e32 v91, 0
	v_mov_b32_e32 v92, 0
	v_mov_b32_e32 v93, 0
	v_mov_b32_e32 v94, 0
	v_mov_b32_e32 v95, 0
	s_mov_b32 s27, 2
.Lhq0_phase:
	s_mov_b32 s26, 0x10000
	s_cmp_eq_u32 s27, 2
	s_cselect_b32 s26, 0x8000, s26
	s_cmp_eq_u32 s27, 3
	s_cselect_b32 s26, 0x5556, s26
	s_cmp_eq_u32 s27, 4
	s_cselect_b32 s26, 0x4000, s26
	v_sub_u32_e32 v2, v51, v46
	v_lshrrev_b32_e32 v2, 3, v2
	v_mul_u32_u24_e32 v2, s26, v2
	v_lshrrev_b32_e32 v2, 16, v2
	v_lshl_add_u32 v5, v2, 3, v46
.Lhq0_s0_top:
	v_sub_u32_e32 v2, v5, v46
	ds_read_b64 v[6:7], v46
	ds_read_b64 v[8:9], v46 offset:8
	ds_read_b64 v[10:11], v46 offset:16
	ds_read_b64 v[12:13], v46 offset:24
	ds_read_b64 v[14:15], v46 offset:32
	ds_read_b64 v[16:17], v46 offset:40
	v_cmp_lt_i32_e64 s[30:31], 0, v2
	s_and_b64 s[30:31], s[30:31], exec
	s_cbranch_scc0 .Lhq0_s0_done
	v_cmp_lt_i32_e64 s[32:33], 8, v2
	v_cmp_lt_i32_e64 s[34:35], 16, v2
	v_cmp_lt_i32_e64 s[36:37], 24, v2
	v_cmp_lt_i32_e64 s[38:39], 32, v2
	v_cmp_lt_i32_e64 s[40:41], 40, v2
	v_cmp_lt_i32_e64 s[42:43], 48, v2
	v_add_u32_e32 v46, 48, v46
	v_min_i32_e32 v46, v46, v5
	s_waitcnt lgkmcnt(0)
	s_mov_b64 exec, s[30:31]
	v_lshlrev_b32_e32 v3, 7, v6
	v_and_or_b32 v3, v3, s29, v1
	global_load_dwordx4 v[18:21], v3, s[8:9]
	s_and_b64 exec, s[32:33], s[32:33]
	s_cbranch_scc0 .Lhq0_s0_ld_done
	v_lshlrev_b32_e32 v4, 7, v8
	v_and_or_b32 v4, v4, s29, v1
	global_load_dwordx4 v[22:25], v4, s[8:9]
	s_and_b64 exec, s[34:35], s[34:35]
	s_cbranch_scc0 .Lhq0_s0_ld_done
	v_lshlrev_b32_e32 v3, 7, v10
	v_and_or_b32 v3, v3, s29, v1
	global_load_dwordx4 v[26:29], v3, s[8:9]
	s_and_b64 exec, s[36:37], s[36:37]
	s_cbranch_scc0 .Lhq0_s0_ld_done
	v_lshlrev_b32_e32 v4, 7, v12
	v_and_or_b32 v4, v4, s29, v1
	global_load_dwordx4 v[30:33], v4, s[8:9]
	s_and_b64 exec, s[38:39], s[38:39]
	s_cbranch_scc0 .Lhq0_s0_ld_done
	v_lshlrev_b32_e32 v3, 7, v14
	v_and_or_b32 v3, v3, s29, v1
	global_load_dwordx4 v[34:37], v3, s[8:9]
	s_and_b64 exec, s[40:41], s[40:41]
	s_cbranch_scc0 .Lhq0_s0_ld_done
	v_lshlrev_b32_e32 v4, 7, v16
	v_and_or_b32 v4, v4, s29, v1
	global_load_dwordx4 v[38:41], v4, s[8:9]
.Lhq0_s0_ld_done:
	s_waitcnt vmcnt(0)
	s_mov_b64 exec, s[30:31]
	v_cvt_f32_f16_e32 v42, v18
	v_cvt_f32_f16_sdwa v43, v18 dst_sel:DWORD dst_unused:UNUSED_PAD src0_sel:WORD_1
	v_cvt_f32_f16_e32 v44, v20
	v_cvt_f32_f16_sdwa v45, v20 dst_sel:DWORD dst_unused:UNUSED_PAD src0_sel:WORD_1
	v_cvt_f32_f16_e32 v18, v19
	v_cvt_f32_f16_sdwa v19, v19 dst_sel:DWORD dst_unused:UNUSED_PAD src0_sel:WORD_1
	v_cvt_f32_f16_e32 v20, v21
	v_cvt_f32_f16_sdwa v21, v21 dst_sel:DWORD dst_unused:UNUSED_PAD src0_sel:WORD_1
	v_fma_f32 v56, v7, v42, v56
	v_fma_f32 v57, v7, v43, v57
	v_fma_f32 v58, v7, v18, v58
	v_fma_f32 v59, v7, v19, v59
	v_fma_f32 v60, v7, v44, v60
	v_fma_f32 v61, v7, v45, v61
	v_fma_f32 v62, v7, v20, v62
	v_fma_f32 v63, v7, v21, v63
	s_and_b64 exec, s[32:33], s[32:33]
	s_cbranch_scc0 .Lhq0_s0_cp_done
	v_cvt_f32_f16_e32 v42, v22
	v_cvt_f32_f16_sdwa v43, v22 dst_sel:DWORD dst_unused:UNUSED_PAD src0_sel:WORD_1
	v_cvt_f32_f16_e32 v44, v24
	v_cvt_f32_f16_sdwa v45, v24 dst_sel:DWORD dst_unused:UNUSED_PAD src0_sel:WORD_1
	v_cvt_f32_f16_e32 v22, v23
	v_cvt_f32_f16_sdwa v23, v23 dst_sel:DWORD dst_unused:UNUSED_PAD src0_sel:WORD_1
	v_cvt_f32_f16_e32 v24, v25
	v_cvt_f32_f16_sdwa v25, v25 dst_sel:DWORD dst_unused:UNUSED_PAD src0_sel:WORD_1
	v_fma_f32 v56, v9, v42, v56
	v_fma_f32 v57, v9, v43, v57
	v_fma_f32 v58, v9, v22, v58
	v_fma_f32 v59, v9, v23, v59
	v_fma_f32 v60, v9, v44, v60
	v_fma_f32 v61, v9, v45, v61
	v_fma_f32 v62, v9, v24, v62
	v_fma_f32 v63, v9, v25, v63
	s_and_b64 exec, s[34:35], s[34:35]
	s_cbranch_scc0 .Lhq0_s0_cp_done
	v_cvt_f32_f16_e32 v42, v26
	v_cvt_f32_f16_sdwa v43, v26 dst_sel:DWORD dst_unused:UNUSED_PAD src0_sel:WORD_1
	v_cvt_f32_f16_e32 v44, v28
	v_cvt_f32_f16_sdwa v45, v28 dst_sel:DWORD dst_unused:UNUSED_PAD src0_sel:WORD_1
	v_cvt_f32_f16_e32 v26, v27
	v_cvt_f32_f16_sdwa v27, v27 dst_sel:DWORD dst_unused:UNUSED_PAD src0_sel:WORD_1
	v_cvt_f32_f16_e32 v28, v29
	v_cvt_f32_f16_sdwa v29, v29 dst_sel:DWORD dst_unused:UNUSED_PAD src0_sel:WORD_1
	v_fma_f32 v56, v11, v42, v56
	v_fma_f32 v57, v11, v43, v57
	v_fma_f32 v58, v11, v26, v58
	v_fma_f32 v59, v11, v27, v59
	v_fma_f32 v60, v11, v44, v60
	v_fma_f32 v61, v11, v45, v61
	v_fma_f32 v62, v11, v28, v62
	v_fma_f32 v63, v11, v29, v63
	s_and_b64 exec, s[36:37], s[36:37]
	s_cbranch_scc0 .Lhq0_s0_cp_done
	v_cvt_f32_f16_e32 v42, v30
	v_cvt_f32_f16_sdwa v43, v30 dst_sel:DWORD dst_unused:UNUSED_PAD src0_sel:WORD_1
	v_cvt_f32_f16_e32 v44, v32
	v_cvt_f32_f16_sdwa v45, v32 dst_sel:DWORD dst_unused:UNUSED_PAD src0_sel:WORD_1
	v_cvt_f32_f16_e32 v30, v31
	v_cvt_f32_f16_sdwa v31, v31 dst_sel:DWORD dst_unused:UNUSED_PAD src0_sel:WORD_1
	v_cvt_f32_f16_e32 v32, v33
	v_cvt_f32_f16_sdwa v33, v33 dst_sel:DWORD dst_unused:UNUSED_PAD src0_sel:WORD_1
	v_fma_f32 v56, v13, v42, v56
	v_fma_f32 v57, v13, v43, v57
	v_fma_f32 v58, v13, v30, v58
	v_fma_f32 v59, v13, v31, v59
	v_fma_f32 v60, v13, v44, v60
	v_fma_f32 v61, v13, v45, v61
	v_fma_f32 v62, v13, v32, v62
	v_fma_f32 v63, v13, v33, v63
	s_and_b64 exec, s[38:39], s[38:39]
	s_cbranch_scc0 .Lhq0_s0_cp_done
	v_cvt_f32_f16_e32 v42, v34
	v_cvt_f32_f16_sdwa v43, v34 dst_sel:DWORD dst_unused:UNUSED_PAD src0_sel:WORD_1
	v_cvt_f32_f16_e32 v44, v36
	v_cvt_f32_f16_sdwa v45, v36 dst_sel:DWORD dst_unused:UNUSED_PAD src0_sel:WORD_1
	v_cvt_f32_f16_e32 v34, v35
	v_cvt_f32_f16_sdwa v35, v35 dst_sel:DWORD dst_unused:UNUSED_PAD src0_sel:WORD_1
	v_cvt_f32_f16_e32 v36, v37
	v_cvt_f32_f16_sdwa v37, v37 dst_sel:DWORD dst_unused:UNUSED_PAD src0_sel:WORD_1
	v_fma_f32 v56, v15, v42, v56
	v_fma_f32 v57, v15, v43, v57
	v_fma_f32 v58, v15, v34, v58
	v_fma_f32 v59, v15, v35, v59
	v_fma_f32 v60, v15, v44, v60
	v_fma_f32 v61, v15, v45, v61
	v_fma_f32 v62, v15, v36, v62
	v_fma_f32 v63, v15, v37, v63
	s_and_b64 exec, s[40:41], s[40:41]
	s_cbranch_scc0 .Lhq0_s0_cp_done
	v_cvt_f32_f16_e32 v42, v38
	v_cvt_f32_f16_sdwa v43, v38 dst_sel:DWORD dst_unused:UNUSED_PAD src0_sel:WORD_1
	v_cvt_f32_f16_e32 v44, v40
	v_cvt_f32_f16_sdwa v45, v40 dst_sel:DWORD dst_unused:UNUSED_PAD src0_sel:WORD_1
	v_cvt_f32_f16_e32 v38, v39
	v_cvt_f32_f16_sdwa v39, v39 dst_sel:DWORD dst_unused:UNUSED_PAD src0_sel:WORD_1
	v_cvt_f32_f16_e32 v40, v41
	v_cvt_f32_f16_sdwa v41, v41 dst_sel:DWORD dst_unused:UNUSED_PAD src0_sel:WORD_1
	v_fma_f32 v56, v17, v42, v56
	v_fma_f32 v57, v17, v43, v57
	v_fma_f32 v58, v17, v38, v58
	v_fma_f32 v59, v17, v39, v59
	v_fma_f32 v60, v17, v44, v60
	v_fma_f32 v61, v17, v45, v61
	v_fma_f32 v62, v17, v40, v62
	v_fma_f32 v63, v17, v41, v63
.Lhq0_s0_cp_done:
	s_and_b64 exec, s[42:43], s[42:43]
	s_cbranch_scc1 .Lhq0_s0_top
.Lhq0_s0_done:
	s_mov_b64 exec, -1
	v_sub_u32_e32 v2, v52, v47
	v_lshrrev_b32_e32 v2, 3, v2
	v_mul_u32_u24_e32 v2, s26, v2
	v_lshrrev_b32_e32 v2, 16, v2
	v_lshl_add_u32 v5, v2, 3, v47
.Lhq0_s1_top:
	v_sub_u32_e32 v2, v5, v47
	ds_read_b64 v[6:7], v47
	ds_read_b64 v[8:9], v47 offset:8
	ds_read_b64 v[10:11], v47 offset:16
	ds_read_b64 v[12:13], v47 offset:24
	ds_read_b64 v[14:15], v47 offset:32
	ds_read_b64 v[16:17], v47 offset:40
	v_cmp_lt_i32_e64 s[30:31], 0, v2
	s_and_b64 s[30:31], s[30:31], exec
	s_cbranch_scc0 .Lhq0_s1_done
	v_cmp_lt_i32_e64 s[32:33], 8, v2
	v_cmp_lt_i32_e64 s[34:35], 16, v2
	v_cmp_lt_i32_e64 s[36:37], 24, v2
	v_cmp_lt_i32_e64 s[38:39], 32, v2
	v_cmp_lt_i32_e64 s[40:41], 40, v2
	v_cmp_lt_i32_e64 s[42:43], 48, v2
	v_add_u32_e32 v47, 48, v47
	v_min_i32_e32 v47, v47, v5
	s_waitcnt lgkmcnt(0)
	s_mov_b64 exec, s[30:31]
	v_lshlrev_b32_e32 v3, 7, v6
	v_and_or_b32 v3, v3, s29, v1
	global_load_dwordx4 v[18:21], v3, s[8:9]
	s_and_b64 exec, s[32:33], s[32:33]
	s_cbranch_scc0 .Lhq0_s1_ld_done
	v_lshlrev_b32_e32 v4, 7, v8
	v_and_or_b32 v4, v4, s29, v1
	global_load_dwordx4 v[22:25], v4, s[8:9]
	s_and_b64 exec, s[34:35], s[34:35]
	s_cbranch_scc0 .Lhq0_s1_ld_done
	v_lshlrev_b32_e32 v3, 7, v10
	v_and_or_b32 v3, v3, s29, v1
	global_load_dwordx4 v[26:29], v3, s[8:9]
	s_and_b64 exec, s[36:37], s[36:37]
	s_cbranch_scc0 .Lhq0_s1_ld_done
	v_lshlrev_b32_e32 v4, 7, v12
	v_and_or_b32 v4, v4, s29, v1
	global_load_dwordx4 v[30:33], v4, s[8:9]
	s_and_b64 exec, s[38:39], s[38:39]
	s_cbranch_scc0 .Lhq0_s1_ld_done
	v_lshlrev_b32_e32 v3, 7, v14
	v_and_or_b32 v3, v3, s29, v1
	global_load_dwordx4 v[34:37], v3, s[8:9]
	s_and_b64 exec, s[40:41], s[40:41]
	s_cbranch_scc0 .Lhq0_s1_ld_done
	v_lshlrev_b32_e32 v4, 7, v16
	v_and_or_b32 v4, v4, s29, v1
	global_load_dwordx4 v[38:41], v4, s[8:9]
.Lhq0_s1_ld_done:
	s_waitcnt vmcnt(0)
	s_mov_b64 exec, s[30:31]
	v_cvt_f32_f16_e32 v42, v18
	v_cvt_f32_f16_sdwa v43, v18 dst_sel:DWORD dst_unused:UNUSED_PAD src0_sel:WORD_1
	v_cvt_f32_f16_e32 v44, v20
	v_cvt_f32_f16_sdwa v45, v20 dst_sel:DWORD dst_unused:UNUSED_PAD src0_sel:WORD_1
	v_cvt_f32_f16_e32 v18, v19
	v_cvt_f32_f16_sdwa v19, v19 dst_sel:DWORD dst_unused:UNUSED_PAD src0_sel:WORD_1
	v_cvt_f32_f16_e32 v20, v21
	v_cvt_f32_f16_sdwa v21, v21 dst_sel:DWORD dst_unused:UNUSED_PAD src0_sel:WORD_1
	v_fma_f32 v64, v7, v42, v64
	v_fma_f32 v65, v7, v43, v65
	v_fma_f32 v66, v7, v18, v66
	v_fma_f32 v67, v7, v19, v67
	v_fma_f32 v68, v7, v44, v68
	v_fma_f32 v69, v7, v45, v69
	v_fma_f32 v70, v7, v20, v70
	v_fma_f32 v71, v7, v21, v71
	s_and_b64 exec, s[32:33], s[32:33]
	s_cbranch_scc0 .Lhq0_s1_cp_done
	v_cvt_f32_f16_e32 v42, v22
	v_cvt_f32_f16_sdwa v43, v22 dst_sel:DWORD dst_unused:UNUSED_PAD src0_sel:WORD_1
	v_cvt_f32_f16_e32 v44, v24
	v_cvt_f32_f16_sdwa v45, v24 dst_sel:DWORD dst_unused:UNUSED_PAD src0_sel:WORD_1
	v_cvt_f32_f16_e32 v22, v23
	v_cvt_f32_f16_sdwa v23, v23 dst_sel:DWORD dst_unused:UNUSED_PAD src0_sel:WORD_1
	v_cvt_f32_f16_e32 v24, v25
	v_cvt_f32_f16_sdwa v25, v25 dst_sel:DWORD dst_unused:UNUSED_PAD src0_sel:WORD_1
	v_fma_f32 v64, v9, v42, v64
	v_fma_f32 v65, v9, v43, v65
	v_fma_f32 v66, v9, v22, v66
	v_fma_f32 v67, v9, v23, v67
	v_fma_f32 v68, v9, v44, v68
	v_fma_f32 v69, v9, v45, v69
	v_fma_f32 v70, v9, v24, v70
	v_fma_f32 v71, v9, v25, v71
	s_and_b64 exec, s[34:35], s[34:35]
	s_cbranch_scc0 .Lhq0_s1_cp_done
	v_cvt_f32_f16_e32 v42, v26
	v_cvt_f32_f16_sdwa v43, v26 dst_sel:DWORD dst_unused:UNUSED_PAD src0_sel:WORD_1
	v_cvt_f32_f16_e32 v44, v28
	v_cvt_f32_f16_sdwa v45, v28 dst_sel:DWORD dst_unused:UNUSED_PAD src0_sel:WORD_1
	v_cvt_f32_f16_e32 v26, v27
	v_cvt_f32_f16_sdwa v27, v27 dst_sel:DWORD dst_unused:UNUSED_PAD src0_sel:WORD_1
	v_cvt_f32_f16_e32 v28, v29
	v_cvt_f32_f16_sdwa v29, v29 dst_sel:DWORD dst_unused:UNUSED_PAD src0_sel:WORD_1
	v_fma_f32 v64, v11, v42, v64
	v_fma_f32 v65, v11, v43, v65
	v_fma_f32 v66, v11, v26, v66
	v_fma_f32 v67, v11, v27, v67
	v_fma_f32 v68, v11, v44, v68
	v_fma_f32 v69, v11, v45, v69
	v_fma_f32 v70, v11, v28, v70
	v_fma_f32 v71, v11, v29, v71
	s_and_b64 exec, s[36:37], s[36:37]
	s_cbranch_scc0 .Lhq0_s1_cp_done
	v_cvt_f32_f16_e32 v42, v30
	v_cvt_f32_f16_sdwa v43, v30 dst_sel:DWORD dst_unused:UNUSED_PAD src0_sel:WORD_1
	v_cvt_f32_f16_e32 v44, v32
	v_cvt_f32_f16_sdwa v45, v32 dst_sel:DWORD dst_unused:UNUSED_PAD src0_sel:WORD_1
	v_cvt_f32_f16_e32 v30, v31
	v_cvt_f32_f16_sdwa v31, v31 dst_sel:DWORD dst_unused:UNUSED_PAD src0_sel:WORD_1
	v_cvt_f32_f16_e32 v32, v33
	v_cvt_f32_f16_sdwa v33, v33 dst_sel:DWORD dst_unused:UNUSED_PAD src0_sel:WORD_1
	v_fma_f32 v64, v13, v42, v64
	v_fma_f32 v65, v13, v43, v65
	v_fma_f32 v66, v13, v30, v66
	v_fma_f32 v67, v13, v31, v67
	v_fma_f32 v68, v13, v44, v68
	v_fma_f32 v69, v13, v45, v69
	v_fma_f32 v70, v13, v32, v70
	v_fma_f32 v71, v13, v33, v71
	s_and_b64 exec, s[38:39], s[38:39]
	s_cbranch_scc0 .Lhq0_s1_cp_done
	v_cvt_f32_f16_e32 v42, v34
	v_cvt_f32_f16_sdwa v43, v34 dst_sel:DWORD dst_unused:UNUSED_PAD src0_sel:WORD_1
	v_cvt_f32_f16_e32 v44, v36
	v_cvt_f32_f16_sdwa v45, v36 dst_sel:DWORD dst_unused:UNUSED_PAD src0_sel:WORD_1
	v_cvt_f32_f16_e32 v34, v35
	v_cvt_f32_f16_sdwa v35, v35 dst_sel:DWORD dst_unused:UNUSED_PAD src0_sel:WORD_1
	v_cvt_f32_f16_e32 v36, v37
	v_cvt_f32_f16_sdwa v37, v37 dst_sel:DWORD dst_unused:UNUSED_PAD src0_sel:WORD_1
	v_fma_f32 v64, v15, v42, v64
	v_fma_f32 v65, v15, v43, v65
	v_fma_f32 v66, v15, v34, v66
	v_fma_f32 v67, v15, v35, v67
	v_fma_f32 v68, v15, v44, v68
	v_fma_f32 v69, v15, v45, v69
	v_fma_f32 v70, v15, v36, v70
	v_fma_f32 v71, v15, v37, v71
	s_and_b64 exec, s[40:41], s[40:41]
	s_cbranch_scc0 .Lhq0_s1_cp_done
	v_cvt_f32_f16_e32 v42, v38
	v_cvt_f32_f16_sdwa v43, v38 dst_sel:DWORD dst_unused:UNUSED_PAD src0_sel:WORD_1
	v_cvt_f32_f16_e32 v44, v40
	v_cvt_f32_f16_sdwa v45, v40 dst_sel:DWORD dst_unused:UNUSED_PAD src0_sel:WORD_1
	v_cvt_f32_f16_e32 v38, v39
	v_cvt_f32_f16_sdwa v39, v39 dst_sel:DWORD dst_unused:UNUSED_PAD src0_sel:WORD_1
	v_cvt_f32_f16_e32 v40, v41
	v_cvt_f32_f16_sdwa v41, v41 dst_sel:DWORD dst_unused:UNUSED_PAD src0_sel:WORD_1
	v_fma_f32 v64, v17, v42, v64
	v_fma_f32 v65, v17, v43, v65
	v_fma_f32 v66, v17, v38, v66
	v_fma_f32 v67, v17, v39, v67
	v_fma_f32 v68, v17, v44, v68
	v_fma_f32 v69, v17, v45, v69
	v_fma_f32 v70, v17, v40, v70
	v_fma_f32 v71, v17, v41, v71

.Lhq0_s1_done:
	s_mov_b64 exec, -1
	v_sub_u32_e32 v2, v53, v48
	v_lshrrev_b32_e32 v2, 3, v2
	v_mul_u32_u24_e32 v2, s26, v2
	v_lshrrev_b32_e32 v2, 16, v2
	v_lshl_add_u32 v5, v2, 3, v48
.Lhq0_s2_top:
	v_sub_u32_e32 v2, v5, v48
	ds_read_b64 v[6:7], v48
	ds_read_b64 v[8:9], v48 offset:8
	ds_read_b64 v[10:11], v48 offset:16
	ds_read_b64 v[12:13], v48 offset:24
	ds_read_b64 v[14:15], v48 offset:32
	ds_read_b64 v[16:17], v48 offset:40
	v_cmp_lt_i32_e64 s[30:31], 0, v2
	s_and_b64 s[30:31], s[30:31], exec
	s_cbranch_scc0 .Lhq0_s2_done
	v_cmp_lt_i32_e64 s[32:33], 8, v2
	v_cmp_lt_i32_e64 s[34:35], 16, v2
	v_cmp_lt_i32_e64 s[36:37], 24, v2
	v_cmp_lt_i32_e64 s[38:39], 32, v2
	v_cmp_lt_i32_e64 s[40:41], 40, v2
	v_cmp_lt_i32_e64 s[42:43], 48, v2
	v_add_u32_e32 v48, 48, v48
	v_min_i32_e32 v48, v48, v5
	s_waitcnt lgkmcnt(0)
	s_mov_b64 exec, s[30:31]
	v_lshlrev_b32_e32 v3, 7, v6
	v_and_or_b32 v3, v3, s29, v1
	global_load_dwordx4 v[18:21], v3, s[8:9]
	s_and_b64 exec, s[32:33], s[32:33]
	s_cbranch_scc0 .Lhq0_s2_ld_done
	v_lshlrev_b32_e32 v4, 7, v8
	v_and_or_b32 v4, v4, s29, v1
	global_load_dwordx4 v[22:25], v4, s[8:9]
	s_and_b64 exec, s[34:35], s[34:35]
	s_cbranch_scc0 .Lhq0_s2_ld_done
	v_lshlrev_b32_e32 v3, 7, v10
	v_and_or_b32 v3, v3, s29, v1
	global_load_dwordx4 v[26:29], v3, s[8:9]
	s_and_b64 exec, s[36:37], s[36:37]
	s_cbranch_scc0 .Lhq0_s2_ld_done
	v_lshlrev_b32_e32 v4, 7, v12
	v_and_or_b32 v4, v4, s29, v1
	global_load_dwordx4 v[30:33], v4, s[8:9]
	s_and_b64 exec, s[38:39], s[38:39]
	s_cbranch_scc0 .Lhq0_s2_ld_done
	v_lshlrev_b32_e32 v3, 7, v14
	v_and_or_b32 v3, v3, s29, v1
	global_load_dwordx4 v[34:37], v3, s[8:9]
	s_and_b64 exec, s[40:41], s[40:41]
	s_cbranch_scc0 .Lhq0_s2_ld_done
	v_lshlrev_b32_e32 v4, 7, v16
	v_and_or_b32 v4, v4, s29, v1
	global_load_dwordx4 v[38:41], v4, s[8:9]
.Lhq0_s2_ld_done:
	s_waitcnt vmcnt(0)
	s_mov_b64 exec, s[30:31]
	v_cvt_f32_f16_e32 v42, v18
	v_cvt_f32_f16_sdwa v43, v18 dst_sel:DWORD dst_unused:UNUSED_PAD src0_sel:WORD_1
	v_cvt_f32_f16_e32 v44, v20
	v_cvt_f32_f16_sdwa v45, v20 dst_sel:DWORD dst_unused:UNUSED_PAD src0_sel:WORD_1
	v_cvt_f32_f16_e32 v18, v19
	v_cvt_f32_f16_sdwa v19, v19 dst_sel:DWORD dst_unused:UNUSED_PAD src0_sel:WORD_1
	v_cvt_f32_f16_e32 v20, v21
	v_cvt_f32_f16_sdwa v21, v21 dst_sel:DWORD dst_unused:UNUSED_PAD src0_sel:WORD_1
	v_fma_f32 v72, v7, v42, v72
	v_fma_f32 v73, v7, v43, v73
	v_fma_f32 v74, v7, v18, v74
	v_fma_f32 v75, v7, v19, v75
	v_fma_f32 v76, v7, v44, v76
	v_fma_f32 v77, v7, v45, v77
	v_fma_f32 v78, v7, v20, v78
	v_fma_f32 v79, v7, v21, v79
	s_and_b64 exec, s[32:33], s[32:33]
	s_cbranch_scc0 .Lhq0_s2_cp_done
	v_cvt_f32_f16_e32 v42, v22
	v_cvt_f32_f16_sdwa v43, v22 dst_sel:DWORD dst_unused:UNUSED_PAD src0_sel:WORD_1
	v_cvt_f32_f16_e32 v44, v24
	v_cvt_f32_f16_sdwa v45, v24 dst_sel:DWORD dst_unused:UNUSED_PAD src0_sel:WORD_1
	v_cvt_f32_f16_e32 v22, v23
	v_cvt_f32_f16_sdwa v23, v23 dst_sel:DWORD dst_unused:UNUSED_PAD src0_sel:WORD_1
	v_cvt_f32_f16_e32 v24, v25
	v_cvt_f32_f16_sdwa v25, v25 dst_sel:DWORD dst_unused:UNUSED_PAD src0_sel:WORD_1
	v_fma_f32 v72, v9, v42, v72
	v_fma_f32 v73, v9, v43, v73
	v_fma_f32 v74, v9, v22, v74
	v_fma_f32 v75, v9, v23, v75
	v_fma_f32 v76, v9, v44, v76
	v_fma_f32 v77, v9, v45, v77
	v_fma_f32 v78, v9, v24, v78
	v_fma_f32 v79, v9, v25, v79
	s_and_b64 exec, s[34:35], s[34:35]
	s_cbranch_scc0 .Lhq0_s2_cp_done
	v_cvt_f32_f16_e32 v42, v26
	v_cvt_f32_f16_sdwa v43, v26 dst_sel:DWORD dst_unused:UNUSED_PAD src0_sel:WORD_1
	v_cvt_f32_f16_e32 v44, v28
	v_cvt_f32_f16_sdwa v45, v28 dst_sel:DWORD dst_unused:UNUSED_PAD src0_sel:WORD_1
	v_cvt_f32_f16_e32 v26, v27
	v_cvt_f32_f16_sdwa v27, v27 dst_sel:DWORD dst_unused:UNUSED_PAD src0_sel:WORD_1
	v_cvt_f32_f16_e32 v28, v29
	v_cvt_f32_f16_sdwa v29, v29 dst_sel:DWORD dst_unused:UNUSED_PAD src0_sel:WORD_1
	v_fma_f32 v72, v11, v42, v72
	v_fma_f32 v73, v11, v43, v73
	v_fma_f32 v74, v11, v26, v74
	v_fma_f32 v75, v11, v27, v75
	v_fma_f32 v76, v11, v44, v76
	v_fma_f32 v77, v11, v45, v77
	v_fma_f32 v78, v11, v28, v78
	v_fma_f32 v79, v11, v29, v79
	s_and_b64 exec, s[36:37], s[36:37]
	s_cbranch_scc0 .Lhq0_s2_cp_done
	v_cvt_f32_f16_e32 v42, v30
	v_cvt_f32_f16_sdwa v43, v30 dst_sel:DWORD dst_unused:UNUSED_PAD src0_sel:WORD_1
	v_cvt_f32_f16_e32 v44, v32
	v_cvt_f32_f16_sdwa v45, v32 dst_sel:DWORD dst_unused:UNUSED_PAD src0_sel:WORD_1
	v_cvt_f32_f16_e32 v30, v31
	v_cvt_f32_f16_sdwa v31, v31 dst_sel:DWORD dst_unused:UNUSED_PAD src0_sel:WORD_1
	v_cvt_f32_f16_e32 v32, v33
	v_cvt_f32_f16_sdwa v33, v33 dst_sel:DWORD dst_unused:UNUSED_PAD src0_sel:WORD_1
	v_fma_f32 v72, v13, v42, v72
	v_fma_f32 v73, v13, v43, v73
	v_fma_f32 v74, v13, v30, v74
	v_fma_f32 v75, v13, v31, v75
	v_fma_f32 v76, v13, v44, v76
	v_fma_f32 v77, v13, v45, v77
	v_fma_f32 v78, v13, v32, v78
	v_fma_f32 v79, v13, v33, v79
	s_and_b64 exec, s[38:39], s[38:39]
	s_cbranch_scc0 .Lhq0_s2_cp_done
	v_cvt_f32_f16_e32 v42, v34
	v_cvt_f32_f16_sdwa v43, v34 dst_sel:DWORD dst_unused:UNUSED_PAD src0_sel:WORD_1
	v_cvt_f32_f16_e32 v44, v36
	v_cvt_f32_f16_sdwa v45, v36 dst_sel:DWORD dst_unused:UNUSED_PAD src0_sel:WORD_1
	v_cvt_f32_f16_e32 v34, v35
	v_cvt_f32_f16_sdwa v35, v35 dst_sel:DWORD dst_unused:UNUSED_PAD src0_sel:WORD_1
	v_cvt_f32_f16_e32 v36, v37
	v_cvt_f32_f16_sdwa v37, v37 dst_sel:DWORD dst_unused:UNUSED_PAD src0_sel:WORD_1
	v_fma_f32 v72, v15, v42, v72
	v_fma_f32 v73, v15, v43, v73
	v_fma_f32 v74, v15, v34, v74
	v_fma_f32 v75, v15, v35, v75
	v_fma_f32 v76, v15, v44, v76
	v_fma_f32 v77, v15, v45, v77
	v_fma_f32 v78, v15, v36, v78
	v_fma_f32 v79, v15, v37, v79
	s_and_b64 exec, s[40:41], s[40:41]
	s_cbranch_scc0 .Lhq0_s2_cp_done
	v_cvt_f32_f16_e32 v42, v38
	v_cvt_f32_f16_sdwa v43, v38 dst_sel:DWORD dst_unused:UNUSED_PAD src0_sel:WORD_1
	v_cvt_f32_f16_e32 v44, v40
	v_cvt_f32_f16_sdwa v45, v40 dst_sel:DWORD dst_unused:UNUSED_PAD src0_sel:WORD_1
	v_cvt_f32_f16_e32 v38, v39
	v_cvt_f32_f16_sdwa v39, v39 dst_sel:DWORD dst_unused:UNUSED_PAD src0_sel:WORD_1
	v_cvt_f32_f16_e32 v40, v41
	v_cvt_f32_f16_sdwa v41, v41 dst_sel:DWORD dst_unused:UNUSED_PAD src0_sel:WORD_1
	v_fma_f32 v72, v17, v42, v72
	v_fma_f32 v73, v17, v43, v73
	v_fma_f32 v74, v17, v38, v74
	v_fma_f32 v75, v17, v39, v75
	v_fma_f32 v76, v17, v44, v76
	v_fma_f32 v77, v17, v45, v77
	v_fma_f32 v78, v17, v40, v78
	v_fma_f32 v79, v17, v41, v79

.Lhq0_s2_done:
	s_mov_b64 exec, -1
	v_sub_u32_e32 v2, v54, v49
	v_lshrrev_b32_e32 v2, 3, v2
	v_mul_u32_u24_e32 v2, s26, v2
	v_lshrrev_b32_e32 v2, 16, v2
	v_lshl_add_u32 v5, v2, 3, v49
.Lhq0_s3_top:
	v_sub_u32_e32 v2, v5, v49
	ds_read_b64 v[6:7], v49
	ds_read_b64 v[8:9], v49 offset:8
	ds_read_b64 v[10:11], v49 offset:16
	ds_read_b64 v[12:13], v49 offset:24
	ds_read_b64 v[14:15], v49 offset:32
	ds_read_b64 v[16:17], v49 offset:40
	v_cmp_lt_i32_e64 s[30:31], 0, v2
	s_and_b64 s[30:31], s[30:31], exec
	s_cbranch_scc0 .Lhq0_s3_done
	v_cmp_lt_i32_e64 s[32:33], 8, v2
	v_cmp_lt_i32_e64 s[34:35], 16, v2
	v_cmp_lt_i32_e64 s[36:37], 24, v2
	v_cmp_lt_i32_e64 s[38:39], 32, v2
	v_cmp_lt_i32_e64 s[40:41], 40, v2
	v_cmp_lt_i32_e64 s[42:43], 48, v2
	v_add_u32_e32 v49, 48, v49
	v_min_i32_e32 v49, v49, v5
	s_waitcnt lgkmcnt(0)
	s_mov_b64 exec, s[30:31]
	v_lshlrev_b32_e32 v3, 7, v6
	v_and_or_b32 v3, v3, s29, v1
	global_load_dwordx4 v[18:21], v3, s[8:9]
	s_and_b64 exec, s[32:33], s[32:33]
	s_cbranch_scc0 .Lhq0_s3_ld_done
	v_lshlrev_b32_e32 v4, 7, v8
	v_and_or_b32 v4, v4, s29, v1
	global_load_dwordx4 v[22:25], v4, s[8:9]
	s_and_b64 exec, s[34:35], s[34:35]
	s_cbranch_scc0 .Lhq0_s3_ld_done
	v_lshlrev_b32_e32 v3, 7, v10
	v_and_or_b32 v3, v3, s29, v1
	global_load_dwordx4 v[26:29], v3, s[8:9]
	s_and_b64 exec, s[36:37], s[36:37]
	s_cbranch_scc0 .Lhq0_s3_ld_done
	v_lshlrev_b32_e32 v4, 7, v12
	v_and_or_b32 v4, v4, s29, v1
	global_load_dwordx4 v[30:33], v4, s[8:9]
	s_and_b64 exec, s[38:39], s[38:39]
	s_cbranch_scc0 .Lhq0_s3_ld_done
	v_lshlrev_b32_e32 v3, 7, v14
	v_and_or_b32 v3, v3, s29, v1
	global_load_dwordx4 v[34:37], v3, s[8:9]
	s_and_b64 exec, s[40:41], s[40:41]
	s_cbranch_scc0 .Lhq0_s3_ld_done
	v_lshlrev_b32_e32 v4, 7, v16
	v_and_or_b32 v4, v4, s29, v1
	global_load_dwordx4 v[38:41], v4, s[8:9]
.Lhq0_s3_ld_done:
	s_waitcnt vmcnt(0)
	s_mov_b64 exec, s[30:31]
	v_cvt_f32_f16_e32 v42, v18
	v_cvt_f32_f16_sdwa v43, v18 dst_sel:DWORD dst_unused:UNUSED_PAD src0_sel:WORD_1
	v_cvt_f32_f16_e32 v44, v20
	v_cvt_f32_f16_sdwa v45, v20 dst_sel:DWORD dst_unused:UNUSED_PAD src0_sel:WORD_1
	v_cvt_f32_f16_e32 v18, v19
	v_cvt_f32_f16_sdwa v19, v19 dst_sel:DWORD dst_unused:UNUSED_PAD src0_sel:WORD_1
	v_cvt_f32_f16_e32 v20, v21
	v_cvt_f32_f16_sdwa v21, v21 dst_sel:DWORD dst_unused:UNUSED_PAD src0_sel:WORD_1
	v_fma_f32 v80, v7, v42, v80
	v_fma_f32 v81, v7, v43, v81
	v_fma_f32 v82, v7, v18, v82
	v_fma_f32 v83, v7, v19, v83
	v_fma_f32 v84, v7, v44, v84
	v_fma_f32 v85, v7, v45, v85
	v_fma_f32 v86, v7, v20, v86
	v_fma_f32 v87, v7, v21, v87
	s_and_b64 exec, s[32:33], s[32:33]
	s_cbranch_scc0 .Lhq0_s3_cp_done
	v_cvt_f32_f16_e32 v42, v22
	v_cvt_f32_f16_sdwa v43, v22 dst_sel:DWORD dst_unused:UNUSED_PAD src0_sel:WORD_1
	v_cvt_f32_f16_e32 v44, v24
	v_cvt_f32_f16_sdwa v45, v24 dst_sel:DWORD dst_unused:UNUSED_PAD src0_sel:WORD_1
	v_cvt_f32_f16_e32 v22, v23
	v_cvt_f32_f16_sdwa v23, v23 dst_sel:DWORD dst_unused:UNUSED_PAD src0_sel:WORD_1
	v_cvt_f32_f16_e32 v24, v25
	v_cvt_f32_f16_sdwa v25, v25 dst_sel:DWORD dst_unused:UNUSED_PAD src0_sel:WORD_1
	v_fma_f32 v80, v9, v42, v80
	v_fma_f32 v81, v9, v43, v81
	v_fma_f32 v82, v9, v22, v82
	v_fma_f32 v83, v9, v23, v83
	v_fma_f32 v84, v9, v44, v84
	v_fma_f32 v85, v9, v45, v85
	v_fma_f32 v86, v9, v24, v86
	v_fma_f32 v87, v9, v25, v87
	s_and_b64 exec, s[34:35], s[34:35]
	s_cbranch_scc0 .Lhq0_s3_cp_done
	v_cvt_f32_f16_e32 v42, v26
	v_cvt_f32_f16_sdwa v43, v26 dst_sel:DWORD dst_unused:UNUSED_PAD src0_sel:WORD_1
	v_cvt_f32_f16_e32 v44, v28
	v_cvt_f32_f16_sdwa v45, v28 dst_sel:DWORD dst_unused:UNUSED_PAD src0_sel:WORD_1
	v_cvt_f32_f16_e32 v26, v27
	v_cvt_f32_f16_sdwa v27, v27 dst_sel:DWORD dst_unused:UNUSED_PAD src0_sel:WORD_1
	v_cvt_f32_f16_e32 v28, v29
	v_cvt_f32_f16_sdwa v29, v29 dst_sel:DWORD dst_unused:UNUSED_PAD src0_sel:WORD_1
	v_fma_f32 v80, v11, v42, v80
	v_fma_f32 v81, v11, v43, v81
	v_fma_f32 v82, v11, v26, v82
	v_fma_f32 v83, v11, v27, v83
	v_fma_f32 v84, v11, v44, v84
	v_fma_f32 v85, v11, v45, v85
	v_fma_f32 v86, v11, v28, v86
	v_fma_f32 v87, v11, v29, v87
	s_and_b64 exec, s[36:37], s[36:37]
	s_cbranch_scc0 .Lhq0_s3_cp_done
	v_cvt_f32_f16_e32 v42, v30
	v_cvt_f32_f16_sdwa v43, v30 dst_sel:DWORD dst_unused:UNUSED_PAD src0_sel:WORD_1
	v_cvt_f32_f16_e32 v44, v32
	v_cvt_f32_f16_sdwa v45, v32 dst_sel:DWORD dst_unused:UNUSED_PAD src0_sel:WORD_1
	v_cvt_f32_f16_e32 v30, v31
	v_cvt_f32_f16_sdwa v31, v31 dst_sel:DWORD dst_unused:UNUSED_PAD src0_sel:WORD_1
	v_cvt_f32_f16_e32 v32, v33
	v_cvt_f32_f16_sdwa v33, v33 dst_sel:DWORD dst_unused:UNUSED_PAD src0_sel:WORD_1
	v_fma_f32 v80, v13, v42, v80
	v_fma_f32 v81, v13, v43, v81
	v_fma_f32 v82, v13, v30, v82
	v_fma_f32 v83, v13, v31, v83
	v_fma_f32 v84, v13, v44, v84
	v_fma_f32 v85, v13, v45, v85
	v_fma_f32 v86, v13, v32, v86
	v_fma_f32 v87, v13, v33, v87
	s_and_b64 exec, s[38:39], s[38:39]
	s_cbranch_scc0 .Lhq0_s3_cp_done
	v_cvt_f32_f16_e32 v42, v34
	v_cvt_f32_f16_sdwa v43, v34 dst_sel:DWORD dst_unused:UNUSED_PAD src0_sel:WORD_1
	v_cvt_f32_f16_e32 v44, v36
	v_cvt_f32_f16_sdwa v45, v36 dst_sel:DWORD dst_unused:UNUSED_PAD src0_sel:WORD_1
	v_cvt_f32_f16_e32 v34, v35
	v_cvt_f32_f16_sdwa v35, v35 dst_sel:DWORD dst_unused:UNUSED_PAD src0_sel:WORD_1
	v_cvt_f32_f16_e32 v36, v37
	v_cvt_f32_f16_sdwa v37, v37 dst_sel:DWORD dst_unused:UNUSED_PAD src0_sel:WORD_1
	v_fma_f32 v80, v15, v42, v80
	v_fma_f32 v81, v15, v43, v81
	v_fma_f32 v82, v15, v34, v82
	v_fma_f32 v83, v15, v35, v83
	v_fma_f32 v84, v15, v44, v84
	v_fma_f32 v85, v15, v45, v85
	v_fma_f32 v86, v15, v36, v86
	v_fma_f32 v87, v15, v37, v87
	s_and_b64 exec, s[40:41], s[40:41]
	s_cbranch_scc0 .Lhq0_s3_cp_done
	v_cvt_f32_f16_e32 v42, v38
	v_cvt_f32_f16_sdwa v43, v38 dst_sel:DWORD dst_unused:UNUSED_PAD src0_sel:WORD_1
	v_cvt_f32_f16_e32 v44, v40
	v_cvt_f32_f16_sdwa v45, v40 dst_sel:DWORD dst_unused:UNUSED_PAD src0_sel:WORD_1
	v_cvt_f32_f16_e32 v38, v39
	v_cvt_f32_f16_sdwa v39, v39 dst_sel:DWORD dst_unused:UNUSED_PAD src0_sel:WORD_1
	v_cvt_f32_f16_e32 v40, v41
	v_cvt_f32_f16_sdwa v41, v41 dst_sel:DWORD dst_unused:UNUSED_PAD src0_sel:WORD_1
	v_fma_f32 v80, v17, v42, v80
	v_fma_f32 v81, v17, v43, v81
	v_fma_f32 v82, v17, v38, v82
	v_fma_f32 v83, v17, v39, v83
	v_fma_f32 v84, v17, v44, v84
	v_fma_f32 v85, v17, v45, v85
	v_fma_f32 v86, v17, v40, v86
	v_fma_f32 v87, v17, v41, v87

.Lhq0_s3_done:
	s_mov_b64 exec, -1
	v_sub_u32_e32 v2, v55, v50
	v_lshrrev_b32_e32 v2, 3, v2
	v_mul_u32_u24_e32 v2, s26, v2
	v_lshrrev_b32_e32 v2, 16, v2
	v_lshl_add_u32 v5, v2, 3, v50
.Lhq0_s4_top:
	v_sub_u32_e32 v2, v5, v50
	ds_read_b64 v[6:7], v50
	ds_read_b64 v[8:9], v50 offset:8
	ds_read_b64 v[10:11], v50 offset:16
	ds_read_b64 v[12:13], v50 offset:24
	ds_read_b64 v[14:15], v50 offset:32
	ds_read_b64 v[16:17], v50 offset:40
	v_cmp_lt_i32_e64 s[30:31], 0, v2
	s_and_b64 s[30:31], s[30:31], exec
	s_cbranch_scc0 .Lhq0_s4_done
	v_cmp_lt_i32_e64 s[32:33], 8, v2
	v_cmp_lt_i32_e64 s[34:35], 16, v2
	v_cmp_lt_i32_e64 s[36:37], 24, v2
	v_cmp_lt_i32_e64 s[38:39], 32, v2
	v_cmp_lt_i32_e64 s[40:41], 40, v2
	v_cmp_lt_i32_e64 s[42:43], 48, v2
	v_add_u32_e32 v50, 48, v50
	v_min_i32_e32 v50, v50, v5
	s_waitcnt lgkmcnt(0)
	s_mov_b64 exec, s[30:31]
	v_lshlrev_b32_e32 v3, 7, v6
	v_and_or_b32 v3, v3, s29, v1
	global_load_dwordx4 v[18:21], v3, s[8:9]
	s_and_b64 exec, s[32:33], s[32:33]
	s_cbranch_scc0 .Lhq0_s4_ld_done
	v_lshlrev_b32_e32 v4, 7, v8
	v_and_or_b32 v4, v4, s29, v1
	global_load_dwordx4 v[22:25], v4, s[8:9]
	s_and_b64 exec, s[34:35], s[34:35]
	s_cbranch_scc0 .Lhq0_s4_ld_done
	v_lshlrev_b32_e32 v3, 7, v10
	v_and_or_b32 v3, v3, s29, v1
	global_load_dwordx4 v[26:29], v3, s[8:9]
	s_and_b64 exec, s[36:37], s[36:37]
	s_cbranch_scc0 .Lhq0_s4_ld_done
	v_lshlrev_b32_e32 v4, 7, v12
	v_and_or_b32 v4, v4, s29, v1
	global_load_dwordx4 v[30:33], v4, s[8:9]
	s_and_b64 exec, s[38:39], s[38:39]
	s_cbranch_scc0 .Lhq0_s4_ld_done
	v_lshlrev_b32_e32 v3, 7, v14
	v_and_or_b32 v3, v3, s29, v1
	global_load_dwordx4 v[34:37], v3, s[8:9]
	s_and_b64 exec, s[40:41], s[40:41]
	s_cbranch_scc0 .Lhq0_s4_ld_done
	v_lshlrev_b32_e32 v4, 7, v16
	v_and_or_b32 v4, v4, s29, v1
	global_load_dwordx4 v[38:41], v4, s[8:9]
.Lhq0_s4_ld_done:
	s_waitcnt vmcnt(0)
	s_mov_b64 exec, s[30:31]
	v_cvt_f32_f16_e32 v42, v18
	v_cvt_f32_f16_sdwa v43, v18 dst_sel:DWORD dst_unused:UNUSED_PAD src0_sel:WORD_1
	v_cvt_f32_f16_e32 v44, v20
	v_cvt_f32_f16_sdwa v45, v20 dst_sel:DWORD dst_unused:UNUSED_PAD src0_sel:WORD_1
	v_cvt_f32_f16_e32 v18, v19
	v_cvt_f32_f16_sdwa v19, v19 dst_sel:DWORD dst_unused:UNUSED_PAD src0_sel:WORD_1
	v_cvt_f32_f16_e32 v20, v21
	v_cvt_f32_f16_sdwa v21, v21 dst_sel:DWORD dst_unused:UNUSED_PAD src0_sel:WORD_1
	v_fma_f32 v88, v7, v42, v88
	v_fma_f32 v89, v7, v43, v89
	v_fma_f32 v90, v7, v18, v90
	v_fma_f32 v91, v7, v19, v91
	v_fma_f32 v92, v7, v44, v92
	v_fma_f32 v93, v7, v45, v93
	v_fma_f32 v94, v7, v20, v94
	v_fma_f32 v95, v7, v21, v95
	s_and_b64 exec, s[32:33], s[32:33]
	s_cbranch_scc0 .Lhq0_s4_cp_done
	v_cvt_f32_f16_e32 v42, v22
	v_cvt_f32_f16_sdwa v43, v22 dst_sel:DWORD dst_unused:UNUSED_PAD src0_sel:WORD_1
	v_cvt_f32_f16_e32 v44, v24
	v_cvt_f32_f16_sdwa v45, v24 dst_sel:DWORD dst_unused:UNUSED_PAD src0_sel:WORD_1
	v_cvt_f32_f16_e32 v22, v23
	v_cvt_f32_f16_sdwa v23, v23 dst_sel:DWORD dst_unused:UNUSED_PAD src0_sel:WORD_1
	v_cvt_f32_f16_e32 v24, v25
	v_cvt_f32_f16_sdwa v25, v25 dst_sel:DWORD dst_unused:UNUSED_PAD src0_sel:WORD_1
	v_fma_f32 v88, v9, v42, v88
	v_fma_f32 v89, v9, v43, v89
	v_fma_f32 v90, v9, v22, v90
	v_fma_f32 v91, v9, v23, v91
	v_fma_f32 v92, v9, v44, v92
	v_fma_f32 v93, v9, v45, v93
	v_fma_f32 v94, v9, v24, v94
	v_fma_f32 v95, v9, v25, v95
	s_and_b64 exec, s[34:35], s[34:35]
	s_cbranch_scc0 .Lhq0_s4_cp_done
	v_cvt_f32_f16_e32 v42, v26
	v_cvt_f32_f16_sdwa v43, v26 dst_sel:DWORD dst_unused:UNUSED_PAD src0_sel:WORD_1
	v_cvt_f32_f16_e32 v44, v28
	v_cvt_f32_f16_sdwa v45, v28 dst_sel:DWORD dst_unused:UNUSED_PAD src0_sel:WORD_1
	v_cvt_f32_f16_e32 v26, v27
	v_cvt_f32_f16_sdwa v27, v27 dst_sel:DWORD dst_unused:UNUSED_PAD src0_sel:WORD_1
	v_cvt_f32_f16_e32 v28, v29
	v_cvt_f32_f16_sdwa v29, v29 dst_sel:DWORD dst_unused:UNUSED_PAD src0_sel:WORD_1
	v_fma_f32 v88, v11, v42, v88
	v_fma_f32 v89, v11, v43, v89
	v_fma_f32 v90, v11, v26, v90
	v_fma_f32 v91, v11, v27, v91
	v_fma_f32 v92, v11, v44, v92
	v_fma_f32 v93, v11, v45, v93
	v_fma_f32 v94, v11, v28, v94
	v_fma_f32 v95, v11, v29, v95
	s_and_b64 exec, s[36:37], s[36:37]
	s_cbranch_scc0 .Lhq0_s4_cp_done
	v_cvt_f32_f16_e32 v42, v30
	v_cvt_f32_f16_sdwa v43, v30 dst_sel:DWORD dst_unused:UNUSED_PAD src0_sel:WORD_1
	v_cvt_f32_f16_e32 v44, v32
	v_cvt_f32_f16_sdwa v45, v32 dst_sel:DWORD dst_unused:UNUSED_PAD src0_sel:WORD_1
	v_cvt_f32_f16_e32 v30, v31
	v_cvt_f32_f16_sdwa v31, v31 dst_sel:DWORD dst_unused:UNUSED_PAD src0_sel:WORD_1
	v_cvt_f32_f16_e32 v32, v33
	v_cvt_f32_f16_sdwa v33, v33 dst_sel:DWORD dst_unused:UNUSED_PAD src0_sel:WORD_1
	v_fma_f32 v88, v13, v42, v88
	v_fma_f32 v89, v13, v43, v89
	v_fma_f32 v90, v13, v30, v90
	v_fma_f32 v91, v13, v31, v91
	v_fma_f32 v92, v13, v44, v92
	v_fma_f32 v93, v13, v45, v93
	v_fma_f32 v94, v13, v32, v94
	v_fma_f32 v95, v13, v33, v95
	s_and_b64 exec, s[38:39], s[38:39]
	s_cbranch_scc0 .Lhq0_s4_cp_done
	v_cvt_f32_f16_e32 v42, v34
	v_cvt_f32_f16_sdwa v43, v34 dst_sel:DWORD dst_unused:UNUSED_PAD src0_sel:WORD_1
	v_cvt_f32_f16_e32 v44, v36
	v_cvt_f32_f16_sdwa v45, v36 dst_sel:DWORD dst_unused:UNUSED_PAD src0_sel:WORD_1
	v_cvt_f32_f16_e32 v34, v35
	v_cvt_f32_f16_sdwa v35, v35 dst_sel:DWORD dst_unused:UNUSED_PAD src0_sel:WORD_1
	v_cvt_f32_f16_e32 v36, v37
	v_cvt_f32_f16_sdwa v37, v37 dst_sel:DWORD dst_unused:UNUSED_PAD src0_sel:WORD_1
	v_fma_f32 v88, v15, v42, v88
	v_fma_f32 v89, v15, v43, v89
	v_fma_f32 v90, v15, v34, v90
	v_fma_f32 v91, v15, v35, v91
	v_fma_f32 v92, v15, v44, v92
	v_fma_f32 v93, v15, v45, v93
	v_fma_f32 v94, v15, v36, v94
	v_fma_f32 v95, v15, v37, v95
	s_and_b64 exec, s[40:41], s[40:41]
	s_cbranch_scc0 .Lhq0_s4_cp_done
	v_cvt_f32_f16_e32 v42, v38
	v_cvt_f32_f16_sdwa v43, v38 dst_sel:DWORD dst_unused:UNUSED_PAD src0_sel:WORD_1
	v_cvt_f32_f16_e32 v44, v40
	v_cvt_f32_f16_sdwa v45, v40 dst_sel:DWORD dst_unused:UNUSED_PAD src0_sel:WORD_1
	v_cvt_f32_f16_e32 v38, v39
	v_cvt_f32_f16_sdwa v39, v39 dst_sel:DWORD dst_unused:UNUSED_PAD src0_sel:WORD_1
	v_cvt_f32_f16_e32 v40, v41
	v_cvt_f32_f16_sdwa v41, v41 dst_sel:DWORD dst_unused:UNUSED_PAD src0_sel:WORD_1
	v_fma_f32 v88, v17, v42, v88
	v_fma_f32 v89, v17, v43, v89
	v_fma_f32 v90, v17, v38, v90
	v_fma_f32 v91, v17, v39, v91
	v_fma_f32 v92, v17, v44, v92
	v_fma_f32 v93, v17, v45, v93
	v_fma_f32 v94, v17, v40, v94
	v_fma_f32 v95, v17, v41, v95

.Lhq0_s4_done:
	s_mov_b64 exec, -1
	s_sub_i32 s27, s27, 1
	s_cmp_gt_u32 s27, 0
	s_cbranch_scc1 .Lhq0_phase
.Lhq0_epilogue:
	v_bfe_u32 v2, v0, 3, 3
	v_lshlrev_b32_e32 v2, 2, v2
	v_add_u32_e32 v2, s28, v2
	ds_read_b32 v46, v2 offset:6720
	ds_read_b32 v47, v2 offset:6752
	ds_read_b32 v48, v2 offset:6784
	ds_read_b32 v49, v2 offset:6816
	ds_read_b32 v50, v2 offset:6848
	s_waitcnt lgkmcnt(0)
	v_add_u32_e32 v46, s15, v46
	v_add_u32_e32 v47, s15, v47
	v_add_u32_e32 v48, s15, v48
	v_add_u32_e32 v49, s15, v49
	v_add_u32_e32 v50, s15, v50
	v_lshlrev_b32_e32 v51, 7, v46
	v_or_b32_e32 v51, v51, v1
	v_cvt_pk_f16_f32 v18, v56, v57
	v_cvt_pk_f16_f32 v19, v58, v59
	v_cvt_pk_f16_f32 v20, v60, v61
	v_cvt_pk_f16_f32 v21, v62, v63
	global_store_dwordx4 v51, v[18:21], s[10:11] nt
	v_lshlrev_b32_e32 v52, 7, v47
	v_or_b32_e32 v52, v52, v1
	v_cvt_pk_f16_f32 v22, v64, v65
	v_cvt_pk_f16_f32 v23, v66, v67
	v_cvt_pk_f16_f32 v24, v68, v69
	v_cvt_pk_f16_f32 v25, v70, v71
	global_store_dwordx4 v52, v[22:25], s[10:11] nt
	v_lshlrev_b32_e32 v53, 7, v48
	v_or_b32_e32 v53, v53, v1
	v_cvt_pk_f16_f32 v26, v72, v73
	v_cvt_pk_f16_f32 v27, v74, v75
	v_cvt_pk_f16_f32 v28, v76, v77
	v_cvt_pk_f16_f32 v29, v78, v79
	global_store_dwordx4 v53, v[26:29], s[10:11] nt
	v_lshlrev_b32_e32 v54, 7, v49
	v_or_b32_e32 v54, v54, v1
	v_cvt_pk_f16_f32 v30, v80, v81
	v_cvt_pk_f16_f32 v31, v82, v83
	v_cvt_pk_f16_f32 v32, v84, v85
	v_cvt_pk_f16_f32 v33, v86, v87
	global_store_dwordx4 v54, v[30:33], s[10:11] nt
	v_lshlrev_b32_e32 v55, 7, v50
	v_or_b32_e32 v55, v55, v1
	v_cvt_pk_f16_f32 v34, v88, v89
	v_cvt_pk_f16_f32 v35, v90, v91
	v_cvt_pk_f16_f32 v36, v92, v93
	v_cvt_pk_f16_f32 v37, v94, v95
	global_store_dwordx4 v55, v[34:37], s[10:11] nt

.Lhq0_fallback:
	v_mov_b32_e32 v56, 0
	v_mov_b32_e32 v57, 0
	v_mov_b32_e32 v58, 0
	v_mov_b32_e32 v59, 0
	v_mov_b32_e32 v60, 0
	v_mov_b32_e32 v61, 0
	v_mov_b32_e32 v62, 0
	v_mov_b32_e32 v63, 0
	v_mov_b32_e32 v64, 0
	v_mov_b32_e32 v65, 0
	v_mov_b32_e32 v66, 0
	v_mov_b32_e32 v67, 0
	v_mov_b32_e32 v68, 0
	v_mov_b32_e32 v69, 0
	v_mov_b32_e32 v70, 0
	v_mov_b32_e32 v71, 0
	v_mov_b32_e32 v72, 0
	v_mov_b32_e32 v73, 0
	v_mov_b32_e32 v74, 0
	v_mov_b32_e32 v75, 0
	v_mov_b32_e32 v76, 0
	v_mov_b32_e32 v77, 0
	v_mov_b32_e32 v78, 0
	v_mov_b32_e32 v79, 0
	v_mov_b32_e32 v80, 0
	v_mov_b32_e32 v81, 0
	v_mov_b32_e32 v82, 0
	v_mov_b32_e32 v83, 0
	v_mov_b32_e32 v84, 0
	v_mov_b32_e32 v85, 0
	v_mov_b32_e32 v86, 0
	v_mov_b32_e32 v87, 0
	v_mov_b32_e32 v88, 0
	v_mov_b32_e32 v89, 0
	v_mov_b32_e32 v90, 0
	v_mov_b32_e32 v91, 0
	v_mov_b32_e32 v92, 0
	v_mov_b32_e32 v93, 0
	v_mov_b32_e32 v94, 0
	v_mov_b32_e32 v95, 0
.Lhq0_fb0_top:
	v_cmp_lt_i32_e32 vcc, v46, v51
	s_and_b64 exec, exec, vcc
	s_cbranch_scc0 .Lhq0_fb0_done
	v_lshlrev_b32_e32 v3, 3, v46
	global_load_dwordx2 v[6:7], v3, s[6:7]
	v_add_u32_e32 v46, 1, v46
	s_waitcnt vmcnt(0)
	v_lshlrev_b32_e32 v4, 7, v6
	v_and_or_b32 v4, v4, s29, v1
	global_load_dwordx4 v[18:21], v4, s[8:9]
	s_waitcnt vmcnt(0)
	v_cvt_f32_f16_e32 v42, v18
	v_cvt_f32_f16_sdwa v43, v18 dst_sel:DWORD dst_unused:UNUSED_PAD src0_sel:WORD_1
	v_cvt_f32_f16_e32 v44, v20
	v_cvt_f32_f16_sdwa v45, v20 dst_sel:DWORD dst_unused:UNUSED_PAD src0_sel:WORD_1
	v_cvt_f32_f16_e32 v18, v19
	v_cvt_f32_f16_sdwa v19, v19 dst_sel:DWORD dst_unused:UNUSED_PAD src0_sel:WORD_1
	v_cvt_f32_f16_e32 v20, v21
	v_cvt_f32_f16_sdwa v21, v21 dst_sel:DWORD dst_unused:UNUSED_PAD src0_sel:WORD_1
	v_fma_f32 v56, v7, v42, v56
	v_fma_f32 v57, v7, v43, v57
	v_fma_f32 v58, v7, v18, v58
	v_fma_f32 v59, v7, v19, v59
	v_fma_f32 v60, v7, v44, v60
	v_fma_f32 v61, v7, v45, v61
	v_fma_f32 v62, v7, v20, v62
	v_fma_f32 v63, v7, v21, v63
	s_branch .Lhq0_fb0_top
.Lhq0_fb0_done:
	s_mov_b64 exec, -1
.Lhq0_fb1_top:
	v_cmp_lt_i32_e32 vcc, v47, v52
	s_and_b64 exec, exec, vcc
	s_cbranch_scc0 .Lhq0_fb1_done
	v_lshlrev_b32_e32 v3, 3, v47
	global_load_dwordx2 v[6:7], v3, s[6:7]
	v_add_u32_e32 v47, 1, v47
	s_waitcnt vmcnt(0)
	v_lshlrev_b32_e32 v4, 7, v6
	v_and_or_b32 v4, v4, s29, v1
	global_load_dwordx4 v[18:21], v4, s[8:9]
	s_waitcnt vmcnt(0)
	v_cvt_f32_f16_e32 v42, v18
	v_cvt_f32_f16_sdwa v43, v18 dst_sel:DWORD dst_unused:UNUSED_PAD src0_sel:WORD_1
	v_cvt_f32_f16_e32 v44, v20
	v_cvt_f32_f16_sdwa v45, v20 dst_sel:DWORD dst_unused:UNUSED_PAD src0_sel:WORD_1
	v_cvt_f32_f16_e32 v18, v19
	v_cvt_f32_f16_sdwa v19, v19 dst_sel:DWORD dst_unused:UNUSED_PAD src0_sel:WORD_1
	v_cvt_f32_f16_e32 v20, v21
	v_cvt_f32_f16_sdwa v21, v21 dst_sel:DWORD dst_unused:UNUSED_PAD src0_sel:WORD_1
	v_fma_f32 v64, v7, v42, v64
	v_fma_f32 v65, v7, v43, v65
	v_fma_f32 v66, v7, v18, v66
	v_fma_f32 v67, v7, v19, v67
	v_fma_f32 v68, v7, v44, v68
	v_fma_f32 v69, v7, v45, v69
	v_fma_f32 v70, v7, v20, v70
	v_fma_f32 v71, v7, v21, v71
	s_branch .Lhq0_fb1_top

.Lhq0_fb2_top:
	v_cmp_lt_i32_e32 vcc, v48, v53
	s_and_b64 exec, exec, vcc
	s_cbranch_scc0 .Lhq0_fb2_done
	v_lshlrev_b32_e32 v3, 3, v48
	global_load_dwordx2 v[6:7], v3, s[6:7]
	v_add_u32_e32 v48, 1, v48
	s_waitcnt vmcnt(0)
	v_lshlrev_b32_e32 v4, 7, v6
	v_and_or_b32 v4, v4, s29, v1
	global_load_dwordx4 v[18:21], v4, s[8:9]
	s_waitcnt vmcnt(0)
	v_cvt_f32_f16_e32 v42, v18
	v_cvt_f32_f16_sdwa v43, v18 dst_sel:DWORD dst_unused:UNUSED_PAD src0_sel:WORD_1
	v_cvt_f32_f16_e32 v44, v20
	v_cvt_f32_f16_sdwa v45, v20 dst_sel:DWORD dst_unused:UNUSED_PAD src0_sel:WORD_1
	v_cvt_f32_f16_e32 v18, v19
	v_cvt_f32_f16_sdwa v19, v19 dst_sel:DWORD dst_unused:UNUSED_PAD src0_sel:WORD_1
	v_cvt_f32_f16_e32 v20, v21
	v_cvt_f32_f16_sdwa v21, v21 dst_sel:DWORD dst_unused:UNUSED_PAD src0_sel:WORD_1
	v_fma_f32 v72, v7, v42, v72
	v_fma_f32 v73, v7, v43, v73
	v_fma_f32 v74, v7, v18, v74
	v_fma_f32 v75, v7, v19, v75
	v_fma_f32 v76, v7, v44, v76
	v_fma_f32 v77, v7, v45, v77
	v_fma_f32 v78, v7, v20, v78
	v_fma_f32 v79, v7, v21, v79
	s_branch .Lhq0_fb2_top

.Lhq0_fb3_top:
	v_cmp_lt_i32_e32 vcc, v49, v54
	s_and_b64 exec, exec, vcc
	s_cbranch_scc0 .Lhq0_fb3_done
	v_lshlrev_b32_e32 v3, 3, v49
	global_load_dwordx2 v[6:7], v3, s[6:7]
	v_add_u32_e32 v49, 1, v49
	s_waitcnt vmcnt(0)
	v_lshlrev_b32_e32 v4, 7, v6
	v_and_or_b32 v4, v4, s29, v1
	global_load_dwordx4 v[18:21], v4, s[8:9]
	s_waitcnt vmcnt(0)
	v_cvt_f32_f16_e32 v42, v18
	v_cvt_f32_f16_sdwa v43, v18 dst_sel:DWORD dst_unused:UNUSED_PAD src0_sel:WORD_1
	v_cvt_f32_f16_e32 v44, v20
	v_cvt_f32_f16_sdwa v45, v20 dst_sel:DWORD dst_unused:UNUSED_PAD src0_sel:WORD_1
	v_cvt_f32_f16_e32 v18, v19
	v_cvt_f32_f16_sdwa v19, v19 dst_sel:DWORD dst_unused:UNUSED_PAD src0_sel:WORD_1
	v_cvt_f32_f16_e32 v20, v21
	v_cvt_f32_f16_sdwa v21, v21 dst_sel:DWORD dst_unused:UNUSED_PAD src0_sel:WORD_1
	v_fma_f32 v80, v7, v42, v80
	v_fma_f32 v81, v7, v43, v81
	v_fma_f32 v82, v7, v18, v82
	v_fma_f32 v83, v7, v19, v83
	v_fma_f32 v84, v7, v44, v84
	v_fma_f32 v85, v7, v45, v85
	v_fma_f32 v86, v7, v20, v86
	v_fma_f32 v87, v7, v21, v87
	s_branch .Lhq0_fb3_top

.Lhq0_fb4_top:
	v_cmp_lt_i32_e32 vcc, v50, v55
	s_and_b64 exec, exec, vcc
	s_cbranch_scc0 .Lhq0_fb4_done
	v_lshlrev_b32_e32 v3, 3, v50
	global_load_dwordx2 v[6:7], v3, s[6:7]
	v_add_u32_e32 v50, 1, v50
	s_waitcnt vmcnt(0)
	v_lshlrev_b32_e32 v4, 7, v6
	v_and_or_b32 v4, v4, s29, v1
	global_load_dwordx4 v[18:21], v4, s[8:9]
	s_waitcnt vmcnt(0)
	v_cvt_f32_f16_e32 v42, v18
	v_cvt_f32_f16_sdwa v43, v18 dst_sel:DWORD dst_unused:UNUSED_PAD src0_sel:WORD_1
	v_cvt_f32_f16_e32 v44, v20
	v_cvt_f32_f16_sdwa v45, v20 dst_sel:DWORD dst_unused:UNUSED_PAD src0_sel:WORD_1
	v_cvt_f32_f16_e32 v18, v19
	v_cvt_f32_f16_sdwa v19, v19 dst_sel:DWORD dst_unused:UNUSED_PAD src0_sel:WORD_1
	v_cvt_f32_f16_e32 v20, v21
	v_cvt_f32_f16_sdwa v21, v21 dst_sel:DWORD dst_unused:UNUSED_PAD src0_sel:WORD_1
	v_fma_f32 v88, v7, v42, v88
	v_fma_f32 v89, v7, v43, v89
	v_fma_f32 v90, v7, v18, v90
	v_fma_f32 v91, v7, v19, v91
	v_fma_f32 v92, v7, v44, v92
	v_fma_f32 v93, v7, v45, v93
	v_fma_f32 v94, v7, v20, v94
	v_fma_f32 v95, v7, v21, v95
	s_branch .Lhq0_fb4_top
.Lhq0_fb4_done:
	s_mov_b64 exec, -1
	s_branch .Lhq0_epilogue
	.p2alignl 8, 3212836864

	.amdhsa_kernel _Z5k_hopILi0EEvPKiPK15HIP_vector_typeIiLj2EEPKS2_IjLj4EEPS6_S8_S8_PKfSB_Pf
		.amdhsa_group_segment_fixed_size 28672
		.amdhsa_private_segment_fixed_size 0
		.amdhsa_kernarg_size 72
		.amdhsa_user_sgpr_count 2
		.amdhsa_user_sgpr_dispatch_ptr 0
		.amdhsa_user_sgpr_queue_ptr 0
		.amdhsa_user_sgpr_kernarg_segment_ptr 1
		.amdhsa_user_sgpr_dispatch_id 0
		.amdhsa_user_sgpr_kernarg_preload_length 0
		.amdhsa_user_sgpr_kernarg_preload_offset 0
		.amdhsa_user_sgpr_private_segment_size 0
		.amdhsa_uses_dynamic_stack 0
		.amdhsa_enable_private_segment 0
		.amdhsa_system_sgpr_workgroup_id_x 1
		.amdhsa_system_sgpr_workgroup_id_y 0
		.amdhsa_system_sgpr_workgroup_id_z 0
		.amdhsa_system_sgpr_workgroup_info 0
		.amdhsa_system_vgpr_workitem_id 0
		.amdhsa_next_free_vgpr 96
		.amdhsa_next_free_sgpr 62
		.amdhsa_accum_offset 96
		.amdhsa_reserve_vcc 1
		.amdhsa_float_round_mode_32 0
		.amdhsa_float_round_mode_16_64 0
		.amdhsa_float_denorm_mode_32 3
		.amdhsa_float_denorm_mode_16_64 3
		.amdhsa_dx10_clamp 1
		.amdhsa_ieee_mode 1
		.amdhsa_fp16_overflow 0
		.amdhsa_tg_split 0
		.amdhsa_exception_fp_ieee_invalid_op 0
		.amdhsa_exception_fp_denorm_src 0
		.amdhsa_exception_fp_ieee_div_zero 0
		.amdhsa_exception_fp_ieee_overflow 0
		.amdhsa_exception_fp_ieee_underflow 0
		.amdhsa_exception_fp_ieee_inexact 0
		.amdhsa_exception_int_div_zero 0
	.end_amdhsa_kernel

_Z5k_hopILi1EEvPKiPK15HIP_vector_typeIiLj2EEPKS2_IjLj4EEPS6_S8_S8_PKfSB_Pf:
	s_lshr_b32 s3, s2, 3
	s_cmpk_gt_u32 s3, 156
	s_cbranch_scc1 .Lhq1_exit
	s_load_dwordx4 s[4:7], s[0:1], 0x0
	s_load_dwordx4 s[8:11], s[0:1], 0x10
	s_load_dwordx4 s[48:51], s[0:1], 0x20
	s_load_dwordx4 s[52:55], s[0:1], 0x30
	s_load_dwordx2 s[56:57], s[0:1], 0x40
	v_lshrrev_b32_e32 v2, 6, v0
	v_and_b32_e32 v3, 63, v0
	s_bfe_u32 s13, s2, 0x10002
	s_and_b32 s14, s2, 3
	v_readfirstlane_b32 s12, v2
	s_lshl_b32 s15, s3, 2
	s_add_i32 s15, s15, s12
	s_mul_i32 s15, s15, 40
	s_mul_i32 s16, s14, 25000
	s_add_i32 s15, s15, s16
	s_add_i32 s16, s16, 24960
	s_min_u32 s15, s15, s16
	v_min_u32_e32 v4, 40, v3
	v_add_u32_e32 v4, s15, v4
	v_lshlrev_b32_e32 v4, 2, v4
	s_mul_i32 s17, s13, 0x61a84
	s_waitcnt lgkmcnt(0)
	s_add_u32 s4, s4, s17
	s_addc_u32 s5, s5, 0
	global_load_dword v5, v4, s[4:5]
	s_mul_i32 s17, s13, 0x927c00
	s_add_u32 s6, s6, s17
	s_addc_u32 s7, s7, 0
	s_mul_i32 s17, s13, 0xc35000
	s_add_u32 s8, s8, s17
	s_addc_u32 s9, s9, 0
	s_add_u32 s48, s48, s17
	s_addc_u32 s49, s49, 0
	s_add_u32 s50, s50, s17
	s_addc_u32 s51, s51, 0
	s_cmp_eq_u32 s13, 0
	s_cselect_b32 s58, s52, s54
	s_cselect_b32 s59, s53, s55
	s_load_dwordx4 s[52:55], s[58:59], 0x0
	s_lshl_b32 s17, s13, 8
	s_add_u32 s56, s56, s17
	s_addc_u32 s57, s57, 0
	s_mul_i32 s28, s12, 6976
	s_mov_b32 s29, 0xffff80
	v_and_b32_e32 v1, 7, v0
	v_lshlrev_b32_e32 v1, 4, v1
	v_lshrrev_b32_e32 v2, 3, v3
	v_lshlrev_b32_e32 v2, 2, v2
	v_lshlrev_b32_e32 v4, 3, v3
	v_add_u32_e32 v6, s28, v4
	v_add_u32_e32 v7, 1, v3
	v_lshlrev_b32_e32 v7, 2, v7
	s_waitcnt vmcnt(0)
	v_readlane_b32 s18, v5, 0
	v_readlane_b32 s19, v5, 40
	ds_bpermute_b32 v8, v7, v5
	s_sub_i32 s20, s19, s18
	s_lshl_b32 s21, s18, 3
	s_add_u32 s22, s6, s21
	s_addc_u32 s23, s7, 0
	s_add_u32 s24, s22, 0x1000
	s_addc_u32 s25, s23, 0
	s_cmpk_gt_i32 s20, 832
	s_cbranch_scc1 .Lhq1_staged
	global_load_dwordx2 v[56:57], v4, s[22:23] offset:0 nt
	s_cmpk_le_i32 s20, 64
	s_cbranch_scc1 .Lhq1_staged
	global_load_dwordx2 v[58:59], v4, s[22:23] offset:512 nt
	s_cmpk_le_i32 s20, 128
	s_cbranch_scc1 .Lhq1_staged
	global_load_dwordx2 v[60:61], v4, s[22:23] offset:1024 nt
	s_cmpk_le_i32 s20, 192
	s_cbranch_scc1 .Lhq1_staged
	global_load_dwordx2 v[62:63], v4, s[22:23] offset:1536 nt
	s_cmpk_le_i32 s20, 256
	s_cbranch_scc1 .Lhq1_staged
	global_load_dwordx2 v[64:65], v4, s[22:23] offset:2048 nt
	s_cmpk_le_i32 s20, 320
	s_cbranch_scc1 .Lhq1_staged
	global_load_dwordx2 v[66:67], v4, s[22:23] offset:2560 nt
	s_cmpk_le_i32 s20, 384
	s_cbranch_scc1 .Lhq1_staged
	global_load_dwordx2 v[68:69], v4, s[22:23] offset:3072 nt
	s_cmpk_le_i32 s20, 448
	s_cbranch_scc1 .Lhq1_staged
	global_load_dwordx2 v[70:71], v4, s[22:23] offset:3584 nt
	s_cmpk_le_i32 s20, 512
	s_cbranch_scc1 .Lhq1_staged
	global_load_dwordx2 v[72:73], v4, s[24:25] offset:0 nt
	s_cmpk_le_i32 s20, 576
	s_cbranch_scc1 .Lhq1_staged
	global_load_dwordx2 v[74:75], v4, s[24:25] offset:512 nt
	s_cmpk_le_i32 s20, 640
	s_cbranch_scc1 .Lhq1_staged
	global_load_dwordx2 v[76:77], v4, s[24:25] offset:1024 nt
	s_cmpk_le_i32 s20, 704
	s_cbranch_scc1 .Lhq1_staged
	global_load_dwordx2 v[78:79], v4, s[24:25] offset:1536 nt
	s_cmpk_le_i32 s20, 768
	s_cbranch_scc1 .Lhq1_staged
	global_load_dwordx2 v[80:81], v4, s[24:25] offset:2048 nt

.Lhq1_epilogue:
	v_bfe_u32 v2, v0, 3, 3
	v_lshlrev_b32_e32 v2, 2, v2
	v_add_u32_e32 v2, s28, v2
	ds_read_b32 v46, v2 offset:6720
	ds_read_b32 v47, v2 offset:6752
	ds_read_b32 v48, v2 offset:6784
	ds_read_b32 v49, v2 offset:6816
	ds_read_b32 v50, v2 offset:6848
	s_waitcnt lgkmcnt(0)
	v_add_u32_e32 v46, s15, v46
	v_add_u32_e32 v47, s15, v47
	v_add_u32_e32 v48, s15, v48
	v_add_u32_e32 v49, s15, v49
	v_add_u32_e32 v50, s15, v50
	s_mov_b32 s46, s55
	v_lshlrev_b32_e32 v3, 7, v46
	v_or_b32_e32 v3, v3, v1
	global_load_dwordx4 v[6:9], v3, s[48:49] nt
	global_load_dwordx4 v[10:13], v3, s[50:51] nt
	global_load_dwordx4 v[14:17], v3, s[8:9]
	v_lshlrev_b32_e32 v4, 7, v47
	v_or_b32_e32 v4, v4, v1
	global_load_dwordx4 v[18:21], v4, s[48:49] nt
	global_load_dwordx4 v[22:25], v4, s[50:51] nt
	global_load_dwordx4 v[26:29], v4, s[8:9]
	s_waitcnt vmcnt(3)
	v_cvt_f32_f16_e32 v38, v6
	v_cvt_f32_f16_sdwa v39, v6 dst_sel:DWORD dst_unused:UNUSED_PAD src0_sel:WORD_1
	v_cvt_f32_f16_e32 v40, v8
	v_cvt_f32_f16_sdwa v41, v8 dst_sel:DWORD dst_unused:UNUSED_PAD src0_sel:WORD_1
	v_cvt_f32_f16_e32 v6, v7
	v_cvt_f32_f16_sdwa v7, v7 dst_sel:DWORD dst_unused:UNUSED_PAD src0_sel:WORD_1
	v_cvt_f32_f16_e32 v8, v9
	v_cvt_f32_f16_sdwa v9, v9 dst_sel:DWORD dst_unused:UNUSED_PAD src0_sel:WORD_1
	v_mul_f32_e32 v30, s52, v38
	v_mul_f32_e32 v31, s52, v39
	v_mul_f32_e32 v32, s52, v6
	v_mul_f32_e32 v33, s52, v7
	v_mul_f32_e32 v34, s52, v40
	v_mul_f32_e32 v35, s52, v41
	v_mul_f32_e32 v36, s52, v8
	v_mul_f32_e32 v37, s52, v9
	v_cvt_f32_f16_e32 v38, v10
	v_cvt_f32_f16_sdwa v39, v10 dst_sel:DWORD dst_unused:UNUSED_PAD src0_sel:WORD_1
	v_cvt_f32_f16_e32 v40, v12
	v_cvt_f32_f16_sdwa v41, v12 dst_sel:DWORD dst_unused:UNUSED_PAD src0_sel:WORD_1
	v_cvt_f32_f16_e32 v10, v11
	v_cvt_f32_f16_sdwa v11, v11 dst_sel:DWORD dst_unused:UNUSED_PAD src0_sel:WORD_1
	v_cvt_f32_f16_e32 v12, v13
	v_cvt_f32_f16_sdwa v13, v13 dst_sel:DWORD dst_unused:UNUSED_PAD src0_sel:WORD_1
	v_fma_f32 v30, s53, v38, v30
	v_fma_f32 v31, s53, v39, v31
	v_fma_f32 v32, s53, v10, v32
	v_fma_f32 v33, s53, v11, v33
	v_fma_f32 v34, s53, v40, v34
	v_fma_f32 v35, s53, v41, v35
	v_fma_f32 v36, s53, v12, v36
	v_fma_f32 v37, s53, v13, v37
	v_cvt_f32_f16_e32 v38, v14
	v_cvt_f32_f16_sdwa v39, v14 dst_sel:DWORD dst_unused:UNUSED_PAD src0_sel:WORD_1
	v_cvt_f32_f16_e32 v40, v16
	v_cvt_f32_f16_sdwa v41, v16 dst_sel:DWORD dst_unused:UNUSED_PAD src0_sel:WORD_1
	v_cvt_f32_f16_e32 v14, v15
	v_cvt_f32_f16_sdwa v15, v15 dst_sel:DWORD dst_unused:UNUSED_PAD src0_sel:WORD_1
	v_cvt_f32_f16_e32 v16, v17
	v_cvt_f32_f16_sdwa v17, v17 dst_sel:DWORD dst_unused:UNUSED_PAD src0_sel:WORD_1
	v_fma_f32 v30, s54, v38, v30
	v_fma_f32 v31, s54, v39, v31
	v_fma_f32 v32, s54, v14, v32
	v_fma_f32 v33, s54, v15, v33
	v_fma_f32 v34, s54, v40, v34
	v_fma_f32 v35, s54, v41, v35
	v_fma_f32 v36, s54, v16, v36
	v_fma_f32 v37, s54, v17, v37
	v_fma_f32 v30, s46, v56, v30
	v_fma_f32 v31, s46, v57, v31
	v_fma_f32 v32, s46, v58, v32
	v_fma_f32 v33, s46, v59, v33
	v_fma_f32 v34, s46, v60, v34
	v_fma_f32 v35, s46, v61, v35
	v_fma_f32 v36, s46, v62, v36
	v_fma_f32 v37, s46, v63, v37
	v_lshlrev_b32_e32 v46, 9, v46
	v_or_b32_e32 v46, v46, v1
	global_store_dwordx4 v46, v[30:33], s[56:57] nt
	global_store_dwordx4 v46, v[34:37], s[56:57] offset:128 nt
	v_lshlrev_b32_e32 v3, 7, v48
	v_or_b32_e32 v3, v3, v1
	global_load_dwordx4 v[6:9], v3, s[48:49] nt
	global_load_dwordx4 v[10:13], v3, s[50:51] nt
	global_load_dwordx4 v[14:17], v3, s[8:9]
	s_waitcnt vmcnt(5)
	v_cvt_f32_f16_e32 v38, v18
	v_cvt_f32_f16_sdwa v39, v18 dst_sel:DWORD dst_unused:UNUSED_PAD src0_sel:WORD_1
	v_cvt_f32_f16_e32 v40, v20
	v_cvt_f32_f16_sdwa v41, v20 dst_sel:DWORD dst_unused:UNUSED_PAD src0_sel:WORD_1
	v_cvt_f32_f16_e32 v18, v19
	v_cvt_f32_f16_sdwa v19, v19 dst_sel:DWORD dst_unused:UNUSED_PAD src0_sel:WORD_1
	v_cvt_f32_f16_e32 v20, v21
	v_cvt_f32_f16_sdwa v21, v21 dst_sel:DWORD dst_unused:UNUSED_PAD src0_sel:WORD_1
	v_mul_f32_e32 v30, s52, v38
	v_mul_f32_e32 v31, s52, v39
	v_mul_f32_e32 v32, s52, v18
	v_mul_f32_e32 v33, s52, v19
	v_mul_f32_e32 v34, s52, v40
	v_mul_f32_e32 v35, s52, v41
	v_mul_f32_e32 v36, s52, v20
	v_mul_f32_e32 v37, s52, v21
	v_cvt_f32_f16_e32 v38, v22
	v_cvt_f32_f16_sdwa v39, v22 dst_sel:DWORD dst_unused:UNUSED_PAD src0_sel:WORD_1
	v_cvt_f32_f16_e32 v40, v24
	v_cvt_f32_f16_sdwa v41, v24 dst_sel:DWORD dst_unused:UNUSED_PAD src0_sel:WORD_1
	v_cvt_f32_f16_e32 v22, v23
	v_cvt_f32_f16_sdwa v23, v23 dst_sel:DWORD dst_unused:UNUSED_PAD src0_sel:WORD_1
	v_cvt_f32_f16_e32 v24, v25
	v_cvt_f32_f16_sdwa v25, v25 dst_sel:DWORD dst_unused:UNUSED_PAD src0_sel:WORD_1
	v_fma_f32 v30, s53, v38, v30
	v_fma_f32 v31, s53, v39, v31
	v_fma_f32 v32, s53, v22, v32
	v_fma_f32 v33, s53, v23, v33
	v_fma_f32 v34, s53, v40, v34
	v_fma_f32 v35, s53, v41, v35
	v_fma_f32 v36, s53, v24, v36
	v_fma_f32 v37, s53, v25, v37
	v_cvt_f32_f16_e32 v38, v26
	v_cvt_f32_f16_sdwa v39, v26 dst_sel:DWORD dst_unused:UNUSED_PAD src0_sel:WORD_1
	v_cvt_f32_f16_e32 v40, v28
	v_cvt_f32_f16_sdwa v41, v28 dst_sel:DWORD dst_unused:UNUSED_PAD src0_sel:WORD_1
	v_cvt_f32_f16_e32 v26, v27
	v_cvt_f32_f16_sdwa v27, v27 dst_sel:DWORD dst_unused:UNUSED_PAD src0_sel:WORD_1
	v_cvt_f32_f16_e32 v28, v29
	v_cvt_f32_f16_sdwa v29, v29 dst_sel:DWORD dst_unused:UNUSED_PAD src0_sel:WORD_1
	v_fma_f32 v30, s54, v38, v30
	v_fma_f32 v31, s54, v39, v31
	v_fma_f32 v32, s54, v26, v32
	v_fma_f32 v33, s54, v27, v33
	v_fma_f32 v34, s54, v40, v34
	v_fma_f32 v35, s54, v41, v35
	v_fma_f32 v36, s54, v28, v36
	v_fma_f32 v37, s54, v29, v37
	v_fma_f32 v30, s46, v64, v30
	v_fma_f32 v31, s46, v65, v31
	v_fma_f32 v32, s46, v66, v32
	v_fma_f32 v33, s46, v67, v33
	v_fma_f32 v34, s46, v68, v34
	v_fma_f32 v35, s46, v69, v35
	v_fma_f32 v36, s46, v70, v36
	v_fma_f32 v37, s46, v71, v37
	v_lshlrev_b32_e32 v47, 9, v47
	v_or_b32_e32 v47, v47, v1
	global_store_dwordx4 v47, v[30:33], s[56:57] nt
	global_store_dwordx4 v47, v[34:37], s[56:57] offset:128 nt
	v_lshlrev_b32_e32 v4, 7, v49
	v_or_b32_e32 v4, v4, v1
	global_load_dwordx4 v[18:21], v4, s[48:49] nt
	global_load_dwordx4 v[22:25], v4, s[50:51] nt
	global_load_dwordx4 v[26:29], v4, s[8:9]
	s_waitcnt vmcnt(5)
	v_cvt_f32_f16_e32 v38, v6
	v_cvt_f32_f16_sdwa v39, v6 dst_sel:DWORD dst_unused:UNUSED_PAD src0_sel:WORD_1
	v_cvt_f32_f16_e32 v40, v8
	v_cvt_f32_f16_sdwa v41, v8 dst_sel:DWORD dst_unused:UNUSED_PAD src0_sel:WORD_1
	v_cvt_f32_f16_e32 v6, v7
	v_cvt_f32_f16_sdwa v7, v7 dst_sel:DWORD dst_unused:UNUSED_PAD src0_sel:WORD_1
	v_cvt_f32_f16_e32 v8, v9
	v_cvt_f32_f16_sdwa v9, v9 dst_sel:DWORD dst_unused:UNUSED_PAD src0_sel:WORD_1
	v_mul_f32_e32 v30, s52, v38
	v_mul_f32_e32 v31, s52, v39
	v_mul_f32_e32 v32, s52, v6
	v_mul_f32_e32 v33, s52, v7
	v_mul_f32_e32 v34, s52, v40
	v_mul_f32_e32 v35, s52, v41
	v_mul_f32_e32 v36, s52, v8
	v_mul_f32_e32 v37, s52, v9
	v_cvt_f32_f16_e32 v38, v10
	v_cvt_f32_f16_sdwa v39, v10 dst_sel:DWORD dst_unused:UNUSED_PAD src0_sel:WORD_1
	v_cvt_f32_f16_e32 v40, v12
	v_cvt_f32_f16_sdwa v41, v12 dst_sel:DWORD dst_unused:UNUSED_PAD src0_sel:WORD_1
	v_cvt_f32_f16_e32 v10, v11
	v_cvt_f32_f16_sdwa v11, v11 dst_sel:DWORD dst_unused:UNUSED_PAD src0_sel:WORD_1
	v_cvt_f32_f16_e32 v12, v13
	v_cvt_f32_f16_sdwa v13, v13 dst_sel:DWORD dst_unused:UNUSED_PAD src0_sel:WORD_1
	v_fma_f32 v30, s53, v38, v30
	v_fma_f32 v31, s53, v39, v31
	v_fma_f32 v32, s53, v10, v32
	v_fma_f32 v33, s53, v11, v33
	v_fma_f32 v34, s53, v40, v34
	v_fma_f32 v35, s53, v41, v35
	v_fma_f32 v36, s53, v12, v36
	v_fma_f32 v37, s53, v13, v37
	v_cvt_f32_f16_e32 v38, v14
	v_cvt_f32_f16_sdwa v39, v14 dst_sel:DWORD dst_unused:UNUSED_PAD src0_sel:WORD_1
	v_cvt_f32_f16_e32 v40, v16
	v_cvt_f32_f16_sdwa v41, v16 dst_sel:DWORD dst_unused:UNUSED_PAD src0_sel:WORD_1
	v_cvt_f32_f16_e32 v14, v15
	v_cvt_f32_f16_sdwa v15, v15 dst_sel:DWORD dst_unused:UNUSED_PAD src0_sel:WORD_1
	v_cvt_f32_f16_e32 v16, v17
	v_cvt_f32_f16_sdwa v17, v17 dst_sel:DWORD dst_unused:UNUSED_PAD src0_sel:WORD_1
	v_fma_f32 v30, s54, v38, v30
	v_fma_f32 v31, s54, v39, v31
	v_fma_f32 v32, s54, v14, v32
	v_fma_f32 v33, s54, v15, v33
	v_fma_f32 v34, s54, v40, v34
	v_fma_f32 v35, s54, v41, v35
	v_fma_f32 v36, s54, v16, v36
	v_fma_f32 v37, s54, v17, v37
	v_fma_f32 v30, s46, v72, v30
	v_fma_f32 v31, s46, v73, v31
	v_fma_f32 v32, s46, v74, v32
	v_fma_f32 v33, s46, v75, v33
	v_fma_f32 v34, s46, v76, v34
	v_fma_f32 v35, s46, v77, v35
	v_fma_f32 v36, s46, v78, v36
	v_fma_f32 v37, s46, v79, v37
	v_lshlrev_b32_e32 v48, 9, v48
	v_or_b32_e32 v48, v48, v1
	global_store_dwordx4 v48, v[30:33], s[56:57] nt
	global_store_dwordx4 v48, v[34:37], s[56:57] offset:128 nt
	v_lshlrev_b32_e32 v3, 7, v50
	v_or_b32_e32 v3, v3, v1
	global_load_dwordx4 v[6:9], v3, s[48:49] nt
	global_load_dwordx4 v[10:13], v3, s[50:51] nt
	global_load_dwordx4 v[14:17], v3, s[8:9]
	s_waitcnt vmcnt(5)
	v_cvt_f32_f16_e32 v38, v18
	v_cvt_f32_f16_sdwa v39, v18 dst_sel:DWORD dst_unused:UNUSED_PAD src0_sel:WORD_1
	v_cvt_f32_f16_e32 v40, v20
	v_cvt_f32_f16_sdwa v41, v20 dst_sel:DWORD dst_unused:UNUSED_PAD src0_sel:WORD_1
	v_cvt_f32_f16_e32 v18, v19
	v_cvt_f32_f16_sdwa v19, v19 dst_sel:DWORD dst_unused:UNUSED_PAD src0_sel:WORD_1
	v_cvt_f32_f16_e32 v20, v21
	v_cvt_f32_f16_sdwa v21, v21 dst_sel:DWORD dst_unused:UNUSED_PAD src0_sel:WORD_1
	v_mul_f32_e32 v30, s52, v38
	v_mul_f32_e32 v31, s52, v39
	v_mul_f32_e32 v32, s52, v18
	v_mul_f32_e32 v33, s52, v19
	v_mul_f32_e32 v34, s52, v40
	v_mul_f32_e32 v35, s52, v41
	v_mul_f32_e32 v36, s52, v20
	v_mul_f32_e32 v37, s52, v21
	v_cvt_f32_f16_e32 v38, v22
	v_cvt_f32_f16_sdwa v39, v22 dst_sel:DWORD dst_unused:UNUSED_PAD src0_sel:WORD_1
	v_cvt_f32_f16_e32 v40, v24
	v_cvt_f32_f16_sdwa v41, v24 dst_sel:DWORD dst_unused:UNUSED_PAD src0_sel:WORD_1
	v_cvt_f32_f16_e32 v22, v23
	v_cvt_f32_f16_sdwa v23, v23 dst_sel:DWORD dst_unused:UNUSED_PAD src0_sel:WORD_1
	v_cvt_f32_f16_e32 v24, v25
	v_cvt_f32_f16_sdwa v25, v25 dst_sel:DWORD dst_unused:UNUSED_PAD src0_sel:WORD_1
	v_fma_f32 v30, s53, v38, v30
	v_fma_f32 v31, s53, v39, v31
	v_fma_f32 v32, s53, v22, v32
	v_fma_f32 v33, s53, v23, v33
	v_fma_f32 v34, s53, v40, v34
	v_fma_f32 v35, s53, v41, v35
	v_fma_f32 v36, s53, v24, v36
	v_fma_f32 v37, s53, v25, v37
	v_cvt_f32_f16_e32 v38, v26
	v_cvt_f32_f16_sdwa v39, v26 dst_sel:DWORD dst_unused:UNUSED_PAD src0_sel:WORD_1
	v_cvt_f32_f16_e32 v40, v28
	v_cvt_f32_f16_sdwa v41, v28 dst_sel:DWORD dst_unused:UNUSED_PAD src0_sel:WORD_1
	v_cvt_f32_f16_e32 v26, v27
	v_cvt_f32_f16_sdwa v27, v27 dst_sel:DWORD dst_unused:UNUSED_PAD src0_sel:WORD_1
	v_cvt_f32_f16_e32 v28, v29
	v_cvt_f32_f16_sdwa v29, v29 dst_sel:DWORD dst_unused:UNUSED_PAD src0_sel:WORD_1
	v_fma_f32 v30, s54, v38, v30
	v_fma_f32 v31, s54, v39, v31
	v_fma_f32 v32, s54, v26, v32
	v_fma_f32 v33, s54, v27, v33
	v_fma_f32 v34, s54, v40, v34
	v_fma_f32 v35, s54, v41, v35
	v_fma_f32 v36, s54, v28, v36
	v_fma_f32 v37, s54, v29, v37
	v_fma_f32 v30, s46, v80, v30
	v_fma_f32 v31, s46, v81, v31
	v_fma_f32 v32, s46, v82, v32
	v_fma_f32 v33, s46, v83, v33
	v_fma_f32 v34, s46, v84, v34
	v_fma_f32 v35, s46, v85, v35
	v_fma_f32 v36, s46, v86, v36
	v_fma_f32 v37, s46, v87, v37
	v_lshlrev_b32_e32 v49, 9, v49
	v_or_b32_e32 v49, v49, v1
	global_store_dwordx4 v49, v[30:33], s[56:57] nt
	global_store_dwordx4 v49, v[34:37], s[56:57] offset:128 nt
	s_waitcnt vmcnt(2)
	v_cvt_f32_f16_e32 v38, v6
	v_cvt_f32_f16_sdwa v39, v6 dst_sel:DWORD dst_unused:UNUSED_PAD src0_sel:WORD_1
	v_cvt_f32_f16_e32 v40, v8
	v_cvt_f32_f16_sdwa v41, v8 dst_sel:DWORD dst_unused:UNUSED_PAD src0_sel:WORD_1
	v_cvt_f32_f16_e32 v6, v7
	v_cvt_f32_f16_sdwa v7, v7 dst_sel:DWORD dst_unused:UNUSED_PAD src0_sel:WORD_1
	v_cvt_f32_f16_e32 v8, v9
	v_cvt_f32_f16_sdwa v9, v9 dst_sel:DWORD dst_unused:UNUSED_PAD src0_sel:WORD_1
	v_mul_f32_e32 v30, s52, v38
	v_mul_f32_e32 v31, s52, v39
	v_mul_f32_e32 v32, s52, v6
	v_mul_f32_e32 v33, s52, v7
	v_mul_f32_e32 v34, s52, v40
	v_mul_f32_e32 v35, s52, v41
	v_mul_f32_e32 v36, s52, v8
	v_mul_f32_e32 v37, s52, v9
	v_cvt_f32_f16_e32 v38, v10
	v_cvt_f32_f16_sdwa v39, v10 dst_sel:DWORD dst_unused:UNUSED_PAD src0_sel:WORD_1
	v_cvt_f32_f16_e32 v40, v12
	v_cvt_f32_f16_sdwa v41, v12 dst_sel:DWORD dst_unused:UNUSED_PAD src0_sel:WORD_1
	v_cvt_f32_f16_e32 v10, v11
	v_cvt_f32_f16_sdwa v11, v11 dst_sel:DWORD dst_unused:UNUSED_PAD src0_sel:WORD_1
	v_cvt_f32_f16_e32 v12, v13
	v_cvt_f32_f16_sdwa v13, v13 dst_sel:DWORD dst_unused:UNUSED_PAD src0_sel:WORD_1
	v_fma_f32 v30, s53, v38, v30
	v_fma_f32 v31, s53, v39, v31
	v_fma_f32 v32, s53, v10, v32
	v_fma_f32 v33, s53, v11, v33
	v_fma_f32 v34, s53, v40, v34
	v_fma_f32 v35, s53, v41, v35
	v_fma_f32 v36, s53, v12, v36
	v_fma_f32 v37, s53, v13, v37
	v_cvt_f32_f16_e32 v38, v14
	v_cvt_f32_f16_sdwa v39, v14 dst_sel:DWORD dst_unused:UNUSED_PAD src0_sel:WORD_1
	v_cvt_f32_f16_e32 v40, v16
	v_cvt_f32_f16_sdwa v41, v16 dst_sel:DWORD dst_unused:UNUSED_PAD src0_sel:WORD_1
	v_cvt_f32_f16_e32 v14, v15
	v_cvt_f32_f16_sdwa v15, v15 dst_sel:DWORD dst_unused:UNUSED_PAD src0_sel:WORD_1
	v_cvt_f32_f16_e32 v16, v17
	v_cvt_f32_f16_sdwa v17, v17 dst_sel:DWORD dst_unused:UNUSED_PAD src0_sel:WORD_1
	v_fma_f32 v30, s54, v38, v30
	v_fma_f32 v31, s54, v39, v31
	v_fma_f32 v32, s54, v14, v32
	v_fma_f32 v33, s54, v15, v33
	v_fma_f32 v34, s54, v40, v34
	v_fma_f32 v35, s54, v41, v35
	v_fma_f32 v36, s54, v16, v36
	v_fma_f32 v37, s54, v17, v37
	v_fma_f32 v30, s46, v88, v30
	v_fma_f32 v31, s46, v89, v31
	v_fma_f32 v32, s46, v90, v32
	v_fma_f32 v33, s46, v91, v33
	v_fma_f32 v34, s46, v92, v34
	v_fma_f32 v35, s46, v93, v35
	v_fma_f32 v36, s46, v94, v36
	v_fma_f32 v37, s46, v95, v37
	v_lshlrev_b32_e32 v50, 9, v50
	v_or_b32_e32 v50, v50, v1
	global_store_dwordx4 v50, v[30:33], s[56:57] nt
	global_store_dwordx4 v50, v[34:37], s[56:57] offset:128 nt

	.amdhsa_kernel _Z5k_hopILi1EEvPKiPK15HIP_vector_typeIiLj2EEPKS2_IjLj4EEPS6_S8_S8_PKfSB_Pf
		.amdhsa_group_segment_fixed_size 28672
		.amdhsa_private_segment_fixed_size 0
		.amdhsa_kernarg_size 72
		.amdhsa_user_sgpr_count 2
		.amdhsa_user_sgpr_dispatch_ptr 0
		.amdhsa_user_sgpr_queue_ptr 0
		.amdhsa_user_sgpr_kernarg_segment_ptr 1
		.amdhsa_user_sgpr_dispatch_id 0
		.amdhsa_user_sgpr_kernarg_preload_length 0
		.amdhsa_user_sgpr_kernarg_preload_offset 0
		.amdhsa_user_sgpr_private_segment_size 0
		.amdhsa_uses_dynamic_stack 0
		.amdhsa_enable_private_segment 0
		.amdhsa_system_sgpr_workgroup_id_x 1
		.amdhsa_system_sgpr_workgroup_id_y 0
		.amdhsa_system_sgpr_workgroup_id_z 0
		.amdhsa_system_sgpr_workgroup_info 0
		.amdhsa_system_vgpr_workitem_id 0
		.amdhsa_next_free_vgpr 96
		.amdhsa_next_free_sgpr 62
		.amdhsa_accum_offset 96
		.amdhsa_reserve_vcc 1
		.amdhsa_float_round_mode_32 0
		.amdhsa_float_round_mode_16_64 0
		.amdhsa_float_denorm_mode_32 3
		.amdhsa_float_denorm_mode_16_64 3
		.amdhsa_dx10_clamp 1
		.amdhsa_ieee_mode 1
		.amdhsa_fp16_overflow 0
		.amdhsa_tg_split 0
		.amdhsa_exception_fp_ieee_invalid_op 0
		.amdhsa_exception_fp_denorm_src 0
		.amdhsa_exception_fp_ieee_div_zero 0
		.amdhsa_exception_fp_ieee_overflow 0
		.amdhsa_exception_fp_ieee_underflow 0
		.amdhsa_exception_fp_ieee_inexact 0
		.amdhsa_exception_int_div_zero 0
	.end_amdhsa_kernel

	.text
	.p2alignl 8, 3212836864
	.fill 256, 4, 3212836864

amdhsa.kernels:
  - .agpr_count:     0
    .args:
      - .actual_access:  read_only
        .address_space:  global
        .offset:         0
        .size:           8
        .value_kind:     global_buffer
      - .actual_access:  read_only
        .address_space:  global
        .offset:         8
        .size:           8
        .value_kind:     global_buffer
      - .actual_access:  read_only
        .address_space:  global
        .offset:         16
        .size:           8
        .value_kind:     global_buffer
      - .actual_access:  read_only
        .address_space:  global
        .offset:         24
        .size:           8
        .value_kind:     global_buffer
      - .actual_access:  write_only
        .address_space:  global
        .offset:         32
        .size:           8
        .value_kind:     global_buffer
      - .actual_access:  write_only
        .address_space:  global
        .offset:         40
        .size:           8
        .value_kind:     global_buffer
    .group_segment_fixed_size: 784
    .kernarg_segment_align: 8
    .kernarg_segment_size: 48
    .language:       OpenCL C
    .language_version:
      - 2
      - 0
    .max_flat_workgroup_size: 256
    .name:           _Z14k_hist_convertPKiS0_PKfS2_PiP15HIP_vector_typeIjLj4EE
    .private_segment_fixed_size: 0
    .sgpr_count:     18
    .sgpr_spill_count: 0
    .symbol:         _Z14k_hist_convertPKiS0_PKfS2_PiP15HIP_vector_typeIjLj4EE.kd
    .uniform_work_group_size: 1
    .uses_dynamic_stack: false
    .vgpr_count:     43
    .vgpr_spill_count: 0
    .wavefront_size: 64
  - .agpr_count:     0
    .args:
      - .actual_access:  read_only
        .address_space:  global
        .offset:         0
        .size:           8
        .value_kind:     global_buffer
      - .actual_access:  read_only
        .address_space:  global
        .offset:         8
        .size:           8
        .value_kind:     global_buffer
      - .actual_access:  read_only
        .address_space:  global
        .offset:         16
        .size:           8
        .value_kind:     global_buffer
      - .actual_access:  read_only
        .address_space:  global
        .offset:         24
        .size:           8
        .value_kind:     global_buffer
      - .actual_access:  read_only
        .address_space:  global
        .offset:         32
        .size:           8
        .value_kind:     global_buffer
      - .actual_access:  read_only
        .address_space:  global
        .offset:         40
        .size:           8
        .value_kind:     global_buffer
      - .actual_access:  read_only
        .address_space:  global
        .offset:         48
        .size:           8
        .value_kind:     global_buffer
      - .actual_access:  write_only
        .address_space:  global
        .offset:         56
        .size:           8
        .value_kind:     global_buffer
      - .actual_access:  write_only
        .address_space:  global
        .offset:         64
        .size:           8
        .value_kind:     global_buffer
    .group_segment_fixed_size: 90432
    .kernarg_segment_align: 8
    .kernarg_segment_size: 72
    .language:       OpenCL C
    .language_version:
      - 2
      - 0
    .max_flat_workgroup_size: 1024
    .name:           _Z16k_bucket_scatterPKiS0_PKfS0_S0_S2_S0_PiP15HIP_vector_typeIiLj2EE
    .private_segment_fixed_size: 0
    .sgpr_count:     30
    .sgpr_spill_count: 0
    .symbol:         _Z16k_bucket_scatterPKiS0_PKfS0_S0_S2_S0_PiP15HIP_vector_typeIiLj2EE.kd
    .uniform_work_group_size: 1
    .uses_dynamic_stack: false
    .vgpr_count:     77
    .vgpr_spill_count: 0
    .wavefront_size: 64
  - .agpr_count:     0
    .args:
      - .actual_access:  read_only
        .address_space:  global
        .offset:         0
        .size:           8
        .value_kind:     global_buffer
      - .actual_access:  read_only
        .address_space:  global
        .offset:         8
        .size:           8
        .value_kind:     global_buffer
      - .actual_access:  write_only
        .address_space:  global
        .offset:         16
        .size:           8
        .value_kind:     global_buffer
      - .actual_access:  write_only
        .address_space:  global
        .offset:         24
        .size:           8
        .value_kind:     global_buffer
    .group_segment_fixed_size: 67616
    .kernarg_segment_align: 8
    .kernarg_segment_size: 32
    .language:       OpenCL C
    .language_version:
      - 2
      - 0
    .max_flat_workgroup_size: 512
    .name:           _Z13k_bucket_sortPKiPK15HIP_vector_typeIiLj2EEPiPS2_
    .private_segment_fixed_size: 0
    .sgpr_count:     102
    .sgpr_spill_count: 0
    .symbol:         _Z13k_bucket_sortPKiPK15HIP_vector_typeIiLj2EEPiPS2_.kd
    .uniform_work_group_size: 1
    .uses_dynamic_stack: false
    .vgpr_count:     97
    .vgpr_spill_count: 0
    .wavefront_size: 64
  - .agpr_count:     0
    .args:
      - .actual_access:  read_only
        .address_space:  global
        .offset:         0
        .size:           8
        .value_kind:     global_buffer
      - .actual_access:  read_only
        .address_space:  global
        .offset:         8
        .size:           8
        .value_kind:     global_buffer
      - .actual_access:  read_only
        .address_space:  global
        .offset:         16
        .size:           8
        .value_kind:     global_buffer
      - .actual_access:  write_only
        .address_space:  global
        .offset:         24
        .size:           8
        .value_kind:     global_buffer
      - .actual_access:  read_only
        .address_space:  global
        .offset:         32
        .size:           8
        .value_kind:     global_buffer
      - .actual_access:  read_only
        .address_space:  global
        .offset:         40
        .size:           8
        .value_kind:     global_buffer
      - .actual_access:  read_only
        .address_space:  global
        .offset:         48
        .size:           8
        .value_kind:     global_buffer
      - .actual_access:  read_only
        .address_space:  global
        .offset:         56
        .size:           8
        .value_kind:     global_buffer
      - .actual_access:  read_only
        .address_space:  global
        .offset:         64
        .size:           8
        .value_kind:     global_buffer
    .group_segment_fixed_size: 28672
    .kernarg_segment_align: 8
    .kernarg_segment_size: 72
    .language:       OpenCL C
    .language_version:
      - 2
      - 0
    .max_flat_workgroup_size: 256
    .name:           _Z5k_hopILi0EEvPKiPK15HIP_vector_typeIiLj2EEPKS2_IjLj4EEPS6_S8_S8_PKfSB_Pf
    .private_segment_fixed_size: 0
    .sgpr_count:     68
    .sgpr_spill_count: 0
    .symbol:         _Z5k_hopILi0EEvPKiPK15HIP_vector_typeIiLj2EEPKS2_IjLj4EEPS6_S8_S8_PKfSB_Pf.kd
    .uniform_work_group_size: 1
    .uses_dynamic_stack: false
    .vgpr_count:     96
    .vgpr_spill_count: 0
    .wavefront_size: 64
  - .agpr_count:     0
    .args:
      - .actual_access:  read_only
        .address_space:  global
        .offset:         0
        .size:           8
        .value_kind:     global_buffer
      - .actual_access:  read_only
        .address_space:  global
        .offset:         8
        .size:           8
        .value_kind:     global_buffer
      - .actual_access:  read_only
        .address_space:  global
        .offset:         16
        .size:           8
        .value_kind:     global_buffer
      - .actual_access:  read_only
        .address_space:  global
        .offset:         24
        .size:           8
        .value_kind:     global_buffer
      - .actual_access:  read_only
        .address_space:  global
        .offset:         32
        .size:           8
        .value_kind:     global_buffer
      - .actual_access:  read_only
        .address_space:  global
        .offset:         40
        .size:           8
        .value_kind:     global_buffer
      - .actual_access:  read_only
        .address_space:  global
        .offset:         48
        .size:           8
        .value_kind:     global_buffer
      - .actual_access:  read_only
        .address_space:  global
        .offset:         56
        .size:           8
        .value_kind:     global_buffer
      - .actual_access:  write_only
        .address_space:  global
        .offset:         64
        .size:           8
        .value_kind:     global_buffer
    .group_segment_fixed_size: 28672
    .kernarg_segment_align: 8
    .kernarg_segment_size: 72
    .language:       OpenCL C
    .language_version:
      - 2
      - 0
    .max_flat_workgroup_size: 256
    .name:           _Z5k_hopILi1EEvPKiPK15HIP_vector_typeIiLj2EEPKS2_IjLj4EEPS6_S8_S8_PKfSB_Pf
    .private_segment_fixed_size: 0
    .sgpr_count:     68
    .sgpr_spill_count: 0
    .symbol:         _Z5k_hopILi1EEvPKiPK15HIP_vector_typeIiLj2EEPKS2_IjLj4EEPS6_S8_S8_PKfSB_Pf.kd
    .uniform_work_group_size: 1
    .uses_dynamic_stack: false
    .vgpr_count:     96
    .vgpr_spill_count: 0
    .wavefront_size: 64
